# grid barrier: waiters poll the top-level arrival counter; XCD leaders no longer bump the per-XCD/top generation flags (nobody polls them) so they skip one atomic round trip before their acquire
# speedup vs baseline: 1.0054x; 1.0054x over previous
; __device__ __forceinline__ unsigned xb_ld(unsigned* p)              { return __hip_atomic_load(p, __ATOMIC_RELAXED, __HIP_MEMORY_SCOPE_AGENT); }
; __device__ __forceinline__ unsigned xb_add(unsigned* p, unsigned v) { return __hip_atomic_fetch_add(p, v, __ATOMIC_RELAXED, __HIP_MEMORY_SCOPE_AGENT); }
; #define XB_SPIN(cond, bar) do { unsigned _sp = 0; while (cond) { __builtin_amdgcn_s_sleep(1); \
;     if ((++_sp & 255u) == 0u) { if (xb_ld(&(bar)[XB_TMO])) break; if (_sp > XB_SPIN_CAP) { atomicAdd(&(bar)[XB_TMO], 1u); break; } } } } while (0)
; __device__ __forceinline__ void xcd_barrier(const XcdBarrier& b) {
;     ...
;         const unsigned old = xb_add(&bar[XB_XSUB(b.x)], 1u);
;         const unsigned gen = old / nloc;
;         if (old + 1u == (gen + 1u) * nloc) {
;             __builtin_amdgcn_fence(__ATOMIC_RELEASE, "agent");
;             asm volatile("s_waitcnt vmcnt(0)" ::: "memory");
;             const unsigned og = xb_add(&bar[XB_TOP], 1u);
;             const unsigned tg = og / nx;
;             if (og + 1u == (tg + 1u) * nx) xb_add(&bar[XB_TOPGEN], 1u);
;             else XB_SPIN(xb_ld(&bar[XB_TOPGEN]) == tg, bar);
.LBB0_112:
	s_or_b64 exec, exec, s[36:37]
	v_cvt_f32_u32_e32 v5, v2
	s_waitcnt vmcnt(0)
	v_readfirstlane_b32 s0, v4
	s_add_u32 s36, s70, 0x4500
	s_addc_u32 s37, s71, 0
	v_rcp_iflag_f32_e32 v5, v5
	v_add_u32_e32 v3, s0, v3
	v_add_u32_e32 v6, 1, v3
	s_mov_b64 s[38:39], 0
	v_mul_f32_e32 v4, 0x4f7ffffe, v5
	v_cvt_u32_f32_e32 v4, v4
	v_sub_u32_e32 v5, 0, v2
	v_mul_lo_u32 v5, v5, v4
	v_mul_hi_u32 v5, v4, v5
	v_add_u32_e32 v4, v4, v5
	v_mul_hi_u32 v4, v3, v4
	v_mul_lo_u32 v5, v4, v2
	v_sub_u32_e32 v3, v3, v5
	v_add_u32_e32 v7, 1, v4
	v_cmp_ge_u32_e32 vcc, v3, v2
	v_sub_u32_e32 v5, v3, v2
	s_nop 0
	v_cndmask_b32_e32 v4, v4, v7, vcc
	v_cndmask_b32_e32 v3, v3, v5, vcc
	v_add_u32_e32 v5, 1, v4
	v_cmp_ge_u32_e32 vcc, v3, v2
	s_nop 1
	v_cndmask_b32_e32 v4, v4, v5, vcc
	v_mul_lo_u32 v3, v2, v4
	v_add_u32_e32 v2, v3, v2
	v_cmp_ne_u32_e32 vcc, v6, v2
	v_mov_b32_e32 v6, v2
	v_mov_b64_e32 v[2:3], s[36:37]
	s_and_saveexec_b64 s[22:23], vcc
	s_cbranch_execz .LBB0_124
	v_mov_b32_e32 v2, 0
	global_load_dword v3, v2, s[36:37] offset:-256 sc1
	s_mov_b64 s[44:45], 0
	s_waitcnt vmcnt(0)
	v_cmp_lt_u32_e32 vcc, v3, v6
	s_and_saveexec_b64 s[42:43], vcc
	s_cbranch_execz .LBB0_123
	s_add_u32 s38, s70, 0x1200
	s_addc_u32 s39, s71, 0
	s_mov_b32 s0, 1
	s_branch .LBB0_116

; __device__ __forceinline__ unsigned xb_ld(unsigned* p)              { return __hip_atomic_load(p, __ATOMIC_RELAXED, __HIP_MEMORY_SCOPE_AGENT); }
; __device__ __forceinline__ unsigned xb_add(unsigned* p, unsigned v) { return __hip_atomic_fetch_add(p, v, __ATOMIC_RELAXED, __HIP_MEMORY_SCOPE_AGENT); }
; #define XB_SPIN(cond, bar) do { unsigned _sp = 0; while (cond) { __builtin_amdgcn_s_sleep(1); \
;     if ((++_sp & 255u) == 0u) { if (xb_ld(&(bar)[XB_TMO])) break; if (_sp > XB_SPIN_CAP) { atomicAdd(&(bar)[XB_TMO], 1u); break; } } } } while (0)
; __device__ __forceinline__ void xcd_barrier(const XcdBarrier& b) {
;     ...
;             xb_add(&bar[XB_XGEN(b.x)], 1u);
;             __builtin_amdgcn_fence(__ATOMIC_ACQUIRE, "agent");
;         } else {
;             XB_SPIN(xb_ld(&bar[XB_XGEN(b.x)]) == gen, bar);
;             __builtin_amdgcn_fence(__ATOMIC_ACQUIRE, "agent");
.LBB0_126:
	s_or_b64 exec, exec, s[22:23]
	s_mov_b64 s[36:37], exec
	v_mbcnt_lo_u32_b32 v2, s36, 0
	v_mbcnt_hi_u32_b32 v2, s37, v2
	v_cmp_eq_u32_e32 vcc, 0, v2
	s_and_saveexec_b64 s[22:23], vcc
	s_cbranch_execz .LBB0_128
	s_bcnt1_i32_b64 s0, s[36:37]
	v_mov_b32_e32 v2, 0x2000
	v_mov_b32_e32 v3, s0
.LBB0_128:
	s_or_b64 exec, exec, s[22:23]
	s_waitcnt vmcnt(0)
	buffer_inv sc1

; __device__ __forceinline__ unsigned xb_ld(unsigned* p)              { return __hip_atomic_load(p, __ATOMIC_RELAXED, __HIP_MEMORY_SCOPE_AGENT); }
; __device__ __forceinline__ unsigned xb_add(unsigned* p, unsigned v) { return __hip_atomic_fetch_add(p, v, __ATOMIC_RELAXED, __HIP_MEMORY_SCOPE_AGENT); }
; #define XB_SPIN(cond, bar) do { unsigned _sp = 0; while (cond) { __builtin_amdgcn_s_sleep(1); \
;     if ((++_sp & 255u) == 0u) { if (xb_ld(&(bar)[XB_TMO])) break; if (_sp > XB_SPIN_CAP) { atomicAdd(&(bar)[XB_TMO], 1u); break; } } } } while (0)
; __device__ __forceinline__ void xcd_barrier(const XcdBarrier& b) {
;     ...
;         const unsigned old = xb_add(&bar[XB_XSUB(b.x)], 1u);
;         const unsigned gen = old / nloc;
;         if (old + 1u == (gen + 1u) * nloc) {
;             __builtin_amdgcn_fence(__ATOMIC_RELEASE, "agent");
;             asm volatile("s_waitcnt vmcnt(0)" ::: "memory");
;             const unsigned og = xb_add(&bar[XB_TOP], 1u);
;             const unsigned tg = og / nx;
;             if (og + 1u == (tg + 1u) * nx) xb_add(&bar[XB_TOPGEN], 1u);
;             else XB_SPIN(xb_ld(&bar[XB_TOPGEN]) == tg, bar);
.LBB0_185:
	s_or_b64 exec, exec, s[42:43]
	v_cvt_f32_u32_e32 v5, v2
	s_waitcnt vmcnt(0)
	v_readfirstlane_b32 s0, v4
	s_add_u32 s42, s70, 0x4500
	s_addc_u32 s43, s71, 0
	v_rcp_iflag_f32_e32 v5, v5
	v_add_u32_e32 v3, s0, v3
	v_add_u32_e32 v6, 1, v3
	s_mov_b64 s[44:45], 0
	v_mul_f32_e32 v4, 0x4f7ffffe, v5
	v_cvt_u32_f32_e32 v4, v4
	v_sub_u32_e32 v5, 0, v2
	v_mul_lo_u32 v5, v5, v4
	v_mul_hi_u32 v5, v4, v5
	v_add_u32_e32 v4, v4, v5
	v_mul_hi_u32 v4, v3, v4
	v_mul_lo_u32 v5, v4, v2
	v_sub_u32_e32 v3, v3, v5
	v_add_u32_e32 v7, 1, v4
	v_cmp_ge_u32_e32 vcc, v3, v2
	v_sub_u32_e32 v5, v3, v2
	s_nop 0
	v_cndmask_b32_e32 v4, v4, v7, vcc
	v_cndmask_b32_e32 v3, v3, v5, vcc
	v_add_u32_e32 v5, 1, v4
	v_cmp_ge_u32_e32 vcc, v3, v2
	s_nop 1
	v_cndmask_b32_e32 v4, v4, v5, vcc
	v_mul_lo_u32 v3, v2, v4
	v_add_u32_e32 v2, v3, v2
	v_cmp_ne_u32_e32 vcc, v6, v2
	v_mov_b32_e32 v6, v2
	v_mov_b64_e32 v[2:3], s[42:43]
	s_and_saveexec_b64 s[38:39], vcc
	s_cbranch_execz .LBB0_197
	v_mov_b32_e32 v2, 0
	global_load_dword v3, v2, s[42:43] offset:-256 sc1
	s_mov_b64 s[50:51], 0
	s_waitcnt vmcnt(0)
	v_cmp_lt_u32_e32 vcc, v3, v6
	s_and_saveexec_b64 s[46:47], vcc
	s_cbranch_execz .LBB0_196
	s_add_u32 s44, s70, 0x1200
	s_addc_u32 s45, s71, 0
	s_mov_b32 s0, 1
	s_branch .LBB0_189

; __device__ __forceinline__ unsigned xb_ld(unsigned* p)              { return __hip_atomic_load(p, __ATOMIC_RELAXED, __HIP_MEMORY_SCOPE_AGENT); }
; __device__ __forceinline__ unsigned xb_add(unsigned* p, unsigned v) { return __hip_atomic_fetch_add(p, v, __ATOMIC_RELAXED, __HIP_MEMORY_SCOPE_AGENT); }
; #define XB_SPIN(cond, bar) do { unsigned _sp = 0; while (cond) { __builtin_amdgcn_s_sleep(1); \
;     if ((++_sp & 255u) == 0u) { if (xb_ld(&(bar)[XB_TMO])) break; if (_sp > XB_SPIN_CAP) { atomicAdd(&(bar)[XB_TMO], 1u); break; } } } } while (0)
; __device__ __forceinline__ void xcd_barrier(const XcdBarrier& b) {
;     ...
;             xb_add(&bar[XB_XGEN(b.x)], 1u);
;             __builtin_amdgcn_fence(__ATOMIC_ACQUIRE, "agent");
;         } else {
;             XB_SPIN(xb_ld(&bar[XB_XGEN(b.x)]) == gen, bar);
;             __builtin_amdgcn_fence(__ATOMIC_ACQUIRE, "agent");
.LBB0_199:
	s_or_b64 exec, exec, s[38:39]
	s_mov_b64 s[42:43], exec
	v_mbcnt_lo_u32_b32 v2, s42, 0
	v_mbcnt_hi_u32_b32 v2, s43, v2
	v_cmp_eq_u32_e32 vcc, 0, v2
	s_and_saveexec_b64 s[38:39], vcc
	s_cbranch_execz .LBB0_201
	s_bcnt1_i32_b64 s0, s[42:43]
	v_mov_b32_e32 v2, 0x2000
	v_mov_b32_e32 v3, s0
.LBB0_201:
	s_or_b64 exec, exec, s[38:39]
	s_waitcnt vmcnt(0)
	buffer_inv sc1

; __device__ __forceinline__ unsigned xb_ld(unsigned* p)              { return __hip_atomic_load(p, __ATOMIC_RELAXED, __HIP_MEMORY_SCOPE_AGENT); }
; __device__ __forceinline__ unsigned xb_add(unsigned* p, unsigned v) { return __hip_atomic_fetch_add(p, v, __ATOMIC_RELAXED, __HIP_MEMORY_SCOPE_AGENT); }
; #define XB_SPIN(cond, bar) do { unsigned _sp = 0; while (cond) { __builtin_amdgcn_s_sleep(1); \
;     if ((++_sp & 255u) == 0u) { if (xb_ld(&(bar)[XB_TMO])) break; if (_sp > XB_SPIN_CAP) { atomicAdd(&(bar)[XB_TMO], 1u); break; } } } } while (0)
; __device__ __forceinline__ void xcd_barrier(const XcdBarrier& b) {
;     ...
;             xb_add(&bar[XB_XGEN(b.x)], 1u);
;             __builtin_amdgcn_fence(__ATOMIC_ACQUIRE, "agent");
;         } else {
;             XB_SPIN(xb_ld(&bar[XB_XGEN(b.x)]) == gen, bar);
;             __builtin_amdgcn_fence(__ATOMIC_ACQUIRE, "agent");
.LBB0_256:
	s_or_b64 exec, exec, s[38:39]
	s_mov_b64 s[42:43], exec
	v_mbcnt_lo_u32_b32 v2, s42, 0
	v_mbcnt_hi_u32_b32 v2, s43, v2
	v_cmp_eq_u32_e32 vcc, 0, v2
	s_and_saveexec_b64 s[38:39], vcc
	s_cbranch_execz .LBB0_258
	s_bcnt1_i32_b64 s0, s[42:43]
	v_mov_b32_e32 v2, 0x2000
	v_mov_b32_e32 v3, s0
.LBB0_258:
	s_or_b64 exec, exec, s[38:39]
	s_waitcnt vmcnt(0)
	buffer_inv sc1

; __device__ __forceinline__ unsigned xb_ld(unsigned* p)              { return __hip_atomic_load(p, __ATOMIC_RELAXED, __HIP_MEMORY_SCOPE_AGENT); }
; __device__ __forceinline__ unsigned xb_add(unsigned* p, unsigned v) { return __hip_atomic_fetch_add(p, v, __ATOMIC_RELAXED, __HIP_MEMORY_SCOPE_AGENT); }
; #define XB_SPIN(cond, bar) do { unsigned _sp = 0; while (cond) { __builtin_amdgcn_s_sleep(1); \
;     if ((++_sp & 255u) == 0u) { if (xb_ld(&(bar)[XB_TMO])) break; if (_sp > XB_SPIN_CAP) { atomicAdd(&(bar)[XB_TMO], 1u); break; } } } } while (0)
; __device__ __forceinline__ void xcd_barrier(const XcdBarrier& b) {
;     ...
;         const unsigned old = xb_add(&bar[XB_XSUB(b.x)], 1u);
;         const unsigned gen = old / nloc;
;         if (old + 1u == (gen + 1u) * nloc) {
;             __builtin_amdgcn_fence(__ATOMIC_RELEASE, "agent");
;             asm volatile("s_waitcnt vmcnt(0)" ::: "memory");
;             const unsigned og = xb_add(&bar[XB_TOP], 1u);
;             const unsigned tg = og / nx;
;             if (og + 1u == (tg + 1u) * nx) xb_add(&bar[XB_TOPGEN], 1u);
;             else XB_SPIN(xb_ld(&bar[XB_TOPGEN]) == tg, bar);
.LBB0_315:
	s_or_b64 exec, exec, s[38:39]
	v_cvt_f32_u32_e32 v5, v2
	s_waitcnt vmcnt(0)
	v_readfirstlane_b32 s0, v4
	s_add_u32 s38, s70, 0x4500
	s_addc_u32 s39, s71, 0
	v_rcp_iflag_f32_e32 v5, v5
	v_add_u32_e32 v3, s0, v3
	v_add_u32_e32 v6, 1, v3
	s_mov_b64 s[42:43], 0
	v_mul_f32_e32 v4, 0x4f7ffffe, v5
	v_cvt_u32_f32_e32 v4, v4
	v_sub_u32_e32 v5, 0, v2
	v_mul_lo_u32 v5, v5, v4
	v_mul_hi_u32 v5, v4, v5
	v_add_u32_e32 v4, v4, v5
	v_mul_hi_u32 v4, v3, v4
	v_mul_lo_u32 v5, v4, v2
	v_sub_u32_e32 v3, v3, v5
	v_add_u32_e32 v7, 1, v4
	v_cmp_ge_u32_e32 vcc, v3, v2
	v_sub_u32_e32 v5, v3, v2
	s_nop 0
	v_cndmask_b32_e32 v4, v4, v7, vcc
	v_cndmask_b32_e32 v3, v3, v5, vcc
	v_add_u32_e32 v5, 1, v4
	v_cmp_ge_u32_e32 vcc, v3, v2
	s_nop 1
	v_cndmask_b32_e32 v4, v4, v5, vcc
	v_mul_lo_u32 v3, v2, v4
	v_add_u32_e32 v2, v3, v2
	v_cmp_ne_u32_e32 vcc, v6, v2
	v_mov_b32_e32 v6, v2
	v_mov_b64_e32 v[2:3], s[38:39]
	s_and_saveexec_b64 s[22:23], vcc
	s_cbranch_execz .LBB0_327
	v_mov_b32_e32 v2, 0
	global_load_dword v3, v2, s[38:39] offset:-256 sc1
	s_mov_b64 s[46:47], 0
	s_waitcnt vmcnt(0)
	v_cmp_lt_u32_e32 vcc, v3, v6
	s_and_saveexec_b64 s[44:45], vcc
	s_cbranch_execz .LBB0_326
	s_add_u32 s42, s70, 0x1200
	s_addc_u32 s43, s71, 0
	s_mov_b32 s0, 1
	s_branch .LBB0_319

; __device__ __forceinline__ unsigned xb_ld(unsigned* p)              { return __hip_atomic_load(p, __ATOMIC_RELAXED, __HIP_MEMORY_SCOPE_AGENT); }
; __device__ __forceinline__ unsigned xb_add(unsigned* p, unsigned v) { return __hip_atomic_fetch_add(p, v, __ATOMIC_RELAXED, __HIP_MEMORY_SCOPE_AGENT); }
; #define XB_SPIN(cond, bar) do { unsigned _sp = 0; while (cond) { __builtin_amdgcn_s_sleep(1); \
;     if ((++_sp & 255u) == 0u) { if (xb_ld(&(bar)[XB_TMO])) break; if (_sp > XB_SPIN_CAP) { atomicAdd(&(bar)[XB_TMO], 1u); break; } } } } while (0)
; __device__ __forceinline__ void xcd_barrier(const XcdBarrier& b) {
;     ...
;             xb_add(&bar[XB_XGEN(b.x)], 1u);
;             __builtin_amdgcn_fence(__ATOMIC_ACQUIRE, "agent");
;         } else {
;             XB_SPIN(xb_ld(&bar[XB_XGEN(b.x)]) == gen, bar);
;             __builtin_amdgcn_fence(__ATOMIC_ACQUIRE, "agent");
.LBB0_329:
	s_or_b64 exec, exec, s[22:23]
	s_mov_b64 s[38:39], exec
	v_mbcnt_lo_u32_b32 v2, s38, 0
	v_mbcnt_hi_u32_b32 v2, s39, v2
	v_cmp_eq_u32_e32 vcc, 0, v2
	s_and_saveexec_b64 s[22:23], vcc
	s_cbranch_execz .LBB0_331
	s_bcnt1_i32_b64 s0, s[38:39]
	v_mov_b32_e32 v2, 0x2000
	v_mov_b32_e32 v3, s0
.LBB0_331:
	s_or_b64 exec, exec, s[22:23]
	s_waitcnt vmcnt(0)
	buffer_inv sc1

; __device__ __forceinline__ unsigned xb_ld(unsigned* p)              { return __hip_atomic_load(p, __ATOMIC_RELAXED, __HIP_MEMORY_SCOPE_AGENT); }
; __device__ __forceinline__ unsigned xb_add(unsigned* p, unsigned v) { return __hip_atomic_fetch_add(p, v, __ATOMIC_RELAXED, __HIP_MEMORY_SCOPE_AGENT); }
; #define XB_SPIN(cond, bar) do { unsigned _sp = 0; while (cond) { __builtin_amdgcn_s_sleep(1); \
;     if ((++_sp & 255u) == 0u) { if (xb_ld(&(bar)[XB_TMO])) break; if (_sp > XB_SPIN_CAP) { atomicAdd(&(bar)[XB_TMO], 1u); break; } } } } while (0)
; __device__ __forceinline__ void xcd_barrier(const XcdBarrier& b) {
;     ...
;         const unsigned old = xb_add(&bar[XB_XSUB(b.x)], 1u);
;         const unsigned gen = old / nloc;
;         if (old + 1u == (gen + 1u) * nloc) {
;             __builtin_amdgcn_fence(__ATOMIC_RELEASE, "agent");
;             asm volatile("s_waitcnt vmcnt(0)" ::: "memory");
;             const unsigned og = xb_add(&bar[XB_TOP], 1u);
;             const unsigned tg = og / nx;
;             if (og + 1u == (tg + 1u) * nx) xb_add(&bar[XB_TOPGEN], 1u);
;             else XB_SPIN(xb_ld(&bar[XB_TOPGEN]) == tg, bar);
.LBB0_373:
	s_or_b64 exec, exec, s[38:39]
	v_cvt_f32_u32_e32 v5, v2
	s_waitcnt vmcnt(0)
	v_readfirstlane_b32 s0, v4
	s_add_u32 s38, s70, 0x4500
	s_addc_u32 s39, s71, 0
	v_rcp_iflag_f32_e32 v5, v5
	v_add_u32_e32 v3, s0, v3
	v_add_u32_e32 v6, 1, v3
	s_mov_b64 s[42:43], 0
	v_mul_f32_e32 v4, 0x4f7ffffe, v5
	v_cvt_u32_f32_e32 v4, v4
	v_sub_u32_e32 v5, 0, v2
	v_mul_lo_u32 v5, v5, v4
	v_mul_hi_u32 v5, v4, v5
	v_add_u32_e32 v4, v4, v5
	v_mul_hi_u32 v4, v3, v4
	v_mul_lo_u32 v5, v4, v2
	v_sub_u32_e32 v3, v3, v5
	v_add_u32_e32 v7, 1, v4
	v_cmp_ge_u32_e32 vcc, v3, v2
	v_sub_u32_e32 v5, v3, v2
	s_nop 0
	v_cndmask_b32_e32 v4, v4, v7, vcc
	v_cndmask_b32_e32 v3, v3, v5, vcc
	v_add_u32_e32 v5, 1, v4
	v_cmp_ge_u32_e32 vcc, v3, v2
	s_nop 1
	v_cndmask_b32_e32 v4, v4, v5, vcc
	v_mul_lo_u32 v3, v2, v4
	v_add_u32_e32 v2, v3, v2
	v_cmp_ne_u32_e32 vcc, v6, v2
	v_mov_b32_e32 v6, v2
	v_mov_b64_e32 v[2:3], s[38:39]
	s_and_saveexec_b64 s[16:17], vcc
	s_cbranch_execz .LBB0_385
	v_mov_b32_e32 v2, 0
	global_load_dword v3, v2, s[38:39] offset:-256 sc1
	s_mov_b64 s[46:47], 0
	s_waitcnt vmcnt(0)
	v_cmp_lt_u32_e32 vcc, v3, v6
	s_and_saveexec_b64 s[44:45], vcc
	s_cbranch_execz .LBB0_384
	s_add_u32 s42, s70, 0x1200
	s_addc_u32 s43, s71, 0
	s_mov_b32 s0, 1
	s_branch .LBB0_377

; __device__ __forceinline__ unsigned xb_ld(unsigned* p)              { return __hip_atomic_load(p, __ATOMIC_RELAXED, __HIP_MEMORY_SCOPE_AGENT); }
; __device__ __forceinline__ unsigned xb_add(unsigned* p, unsigned v) { return __hip_atomic_fetch_add(p, v, __ATOMIC_RELAXED, __HIP_MEMORY_SCOPE_AGENT); }
; #define XB_SPIN(cond, bar) do { unsigned _sp = 0; while (cond) { __builtin_amdgcn_s_sleep(1); \
;     if ((++_sp & 255u) == 0u) { if (xb_ld(&(bar)[XB_TMO])) break; if (_sp > XB_SPIN_CAP) { atomicAdd(&(bar)[XB_TMO], 1u); break; } } } } while (0)
; __device__ __forceinline__ void xcd_barrier(const XcdBarrier& b) {
;     ...
;             xb_add(&bar[XB_XGEN(b.x)], 1u);
;             __builtin_amdgcn_fence(__ATOMIC_ACQUIRE, "agent");
;         } else {
;             XB_SPIN(xb_ld(&bar[XB_XGEN(b.x)]) == gen, bar);
;             __builtin_amdgcn_fence(__ATOMIC_ACQUIRE, "agent");
.LBB0_387:
	s_or_b64 exec, exec, s[16:17]
	s_mov_b64 s[38:39], exec
	v_mbcnt_lo_u32_b32 v2, s38, 0
	v_mbcnt_hi_u32_b32 v2, s39, v2
	v_cmp_eq_u32_e32 vcc, 0, v2
	s_and_saveexec_b64 s[16:17], vcc
	s_cbranch_execz .LBB0_389
	s_bcnt1_i32_b64 s0, s[38:39]
	v_mov_b32_e32 v2, 0x2000
	v_mov_b32_e32 v3, s0
.LBB0_389:
	s_or_b64 exec, exec, s[16:17]
	s_waitcnt vmcnt(0)
	buffer_inv sc1

; __device__ __forceinline__ unsigned xb_ld(unsigned* p)              { return __hip_atomic_load(p, __ATOMIC_RELAXED, __HIP_MEMORY_SCOPE_AGENT); }
; __device__ __forceinline__ unsigned xb_add(unsigned* p, unsigned v) { return __hip_atomic_fetch_add(p, v, __ATOMIC_RELAXED, __HIP_MEMORY_SCOPE_AGENT); }
; #define XB_SPIN(cond, bar) do { unsigned _sp = 0; while (cond) { __builtin_amdgcn_s_sleep(1); \
;     if ((++_sp & 255u) == 0u) { if (xb_ld(&(bar)[XB_TMO])) break; if (_sp > XB_SPIN_CAP) { atomicAdd(&(bar)[XB_TMO], 1u); break; } } } } while (0)
; __device__ __forceinline__ void xcd_barrier(const XcdBarrier& b) {
;     ...
;             xb_add(&bar[XB_XGEN(b.x)], 1u);
;             __builtin_amdgcn_fence(__ATOMIC_ACQUIRE, "agent");
;         } else {
;             XB_SPIN(xb_ld(&bar[XB_XGEN(b.x)]) == gen, bar);
;             __builtin_amdgcn_fence(__ATOMIC_ACQUIRE, "agent");
.LBB0_453:
	s_or_b64 exec, exec, s[16:17]
	s_mov_b64 s[38:39], exec
	v_mbcnt_lo_u32_b32 v2, s38, 0
	v_mbcnt_hi_u32_b32 v2, s39, v2
	v_cmp_eq_u32_e32 vcc, 0, v2
	s_and_saveexec_b64 s[16:17], vcc
	s_cbranch_execz .LBB0_455
	s_bcnt1_i32_b64 s0, s[38:39]
	v_mov_b32_e32 v2, 0x2000
	v_mov_b32_e32 v3, s0
.LBB0_455:
	s_or_b64 exec, exec, s[16:17]
	s_waitcnt vmcnt(0)
	buffer_inv sc1

; __device__ __forceinline__ unsigned xb_ld(unsigned* p)              { return __hip_atomic_load(p, __ATOMIC_RELAXED, __HIP_MEMORY_SCOPE_AGENT); }
; __device__ __forceinline__ unsigned xb_add(unsigned* p, unsigned v) { return __hip_atomic_fetch_add(p, v, __ATOMIC_RELAXED, __HIP_MEMORY_SCOPE_AGENT); }
; #define XB_SPIN(cond, bar) do { unsigned _sp = 0; while (cond) { __builtin_amdgcn_s_sleep(1); \
;     if ((++_sp & 255u) == 0u) { if (xb_ld(&(bar)[XB_TMO])) break; if (_sp > XB_SPIN_CAP) { atomicAdd(&(bar)[XB_TMO], 1u); break; } } } } while (0)
; __device__ __forceinline__ void xcd_barrier(const XcdBarrier& b) {
;     ...
;         const unsigned old = xb_add(&bar[XB_XSUB(b.x)], 1u);
;         const unsigned gen = old / nloc;
;         if (old + 1u == (gen + 1u) * nloc) {
;             __builtin_amdgcn_fence(__ATOMIC_RELEASE, "agent");
;             asm volatile("s_waitcnt vmcnt(0)" ::: "memory");
;             const unsigned og = xb_add(&bar[XB_TOP], 1u);
;             const unsigned tg = og / nx;
;             if (og + 1u == (tg + 1u) * nx) xb_add(&bar[XB_TOPGEN], 1u);
;             else XB_SPIN(xb_ld(&bar[XB_TOPGEN]) == tg, bar);
.LBB0_511:
	s_or_b64 exec, exec, s[44:45]
	v_cvt_f32_u32_e32 v5, v2
	s_waitcnt vmcnt(0)
	v_readfirstlane_b32 s0, v4
	s_add_u32 s44, s70, 0x4500
	s_addc_u32 s45, s71, 0
	v_rcp_iflag_f32_e32 v5, v5
	v_add_u32_e32 v3, s0, v3
	v_add_u32_e32 v6, 1, v3
	s_mov_b64 s[46:47], 0
	v_mul_f32_e32 v4, 0x4f7ffffe, v5
	v_cvt_u32_f32_e32 v4, v4
	v_sub_u32_e32 v5, 0, v2
	v_mul_lo_u32 v5, v5, v4
	v_mul_hi_u32 v5, v4, v5
	v_add_u32_e32 v4, v4, v5
	v_mul_hi_u32 v4, v3, v4
	v_mul_lo_u32 v5, v4, v2
	v_sub_u32_e32 v3, v3, v5
	v_add_u32_e32 v7, 1, v4
	v_cmp_ge_u32_e32 vcc, v3, v2
	v_sub_u32_e32 v5, v3, v2
	s_nop 0
	v_cndmask_b32_e32 v4, v4, v7, vcc
	v_cndmask_b32_e32 v3, v3, v5, vcc
	v_add_u32_e32 v5, 1, v4
	v_cmp_ge_u32_e32 vcc, v3, v2
	s_nop 1
	v_cndmask_b32_e32 v4, v4, v5, vcc
	v_mul_lo_u32 v3, v2, v4
	v_add_u32_e32 v2, v3, v2
	v_cmp_ne_u32_e32 vcc, v6, v2
	v_mov_b32_e32 v6, v2
	v_mov_b64_e32 v[2:3], s[44:45]
	s_and_saveexec_b64 s[42:43], vcc
	s_cbranch_execz .LBB0_523
	v_mov_b32_e32 v2, 0
	global_load_dword v3, v2, s[44:45] offset:-256 sc1
	s_mov_b64 s[52:53], 0
	s_waitcnt vmcnt(0)
	v_cmp_lt_u32_e32 vcc, v3, v6
	s_and_saveexec_b64 s[50:51], vcc
	s_cbranch_execz .LBB0_522
	s_add_u32 s46, s70, 0x1200
	s_addc_u32 s47, s71, 0
	s_mov_b32 s0, 1
	s_branch .LBB0_515

; __device__ __forceinline__ unsigned xb_ld(unsigned* p)              { return __hip_atomic_load(p, __ATOMIC_RELAXED, __HIP_MEMORY_SCOPE_AGENT); }
; __device__ __forceinline__ unsigned xb_add(unsigned* p, unsigned v) { return __hip_atomic_fetch_add(p, v, __ATOMIC_RELAXED, __HIP_MEMORY_SCOPE_AGENT); }
; #define XB_SPIN(cond, bar) do { unsigned _sp = 0; while (cond) { __builtin_amdgcn_s_sleep(1); \
;     if ((++_sp & 255u) == 0u) { if (xb_ld(&(bar)[XB_TMO])) break; if (_sp > XB_SPIN_CAP) { atomicAdd(&(bar)[XB_TMO], 1u); break; } } } } while (0)
; __device__ __forceinline__ void xcd_barrier(const XcdBarrier& b) {
;     ...
;             xb_add(&bar[XB_XGEN(b.x)], 1u);
;             __builtin_amdgcn_fence(__ATOMIC_ACQUIRE, "agent");
;         } else {
;             XB_SPIN(xb_ld(&bar[XB_XGEN(b.x)]) == gen, bar);
;             __builtin_amdgcn_fence(__ATOMIC_ACQUIRE, "agent");
.LBB0_525:
	s_or_b64 exec, exec, s[42:43]
	s_mov_b64 s[44:45], exec
	v_mbcnt_lo_u32_b32 v2, s44, 0
	v_mbcnt_hi_u32_b32 v2, s45, v2
	v_cmp_eq_u32_e32 vcc, 0, v2
	s_and_saveexec_b64 s[42:43], vcc
	s_cbranch_execz .LBB0_527
	s_bcnt1_i32_b64 s0, s[44:45]
	v_mov_b32_e32 v2, 0x2000
	v_mov_b32_e32 v3, s0
.LBB0_527:
	s_or_b64 exec, exec, s[42:43]
	s_waitcnt vmcnt(0)
	buffer_inv sc1

; __device__ __forceinline__ unsigned xb_ld(unsigned* p)              { return __hip_atomic_load(p, __ATOMIC_RELAXED, __HIP_MEMORY_SCOPE_AGENT); }
; __device__ __forceinline__ unsigned xb_add(unsigned* p, unsigned v) { return __hip_atomic_fetch_add(p, v, __ATOMIC_RELAXED, __HIP_MEMORY_SCOPE_AGENT); }
; #define XB_SPIN(cond, bar) do { unsigned _sp = 0; while (cond) { __builtin_amdgcn_s_sleep(1); \
;     if ((++_sp & 255u) == 0u) { if (xb_ld(&(bar)[XB_TMO])) break; if (_sp > XB_SPIN_CAP) { atomicAdd(&(bar)[XB_TMO], 1u); break; } } } } while (0)
; __device__ __forceinline__ void xcd_barrier(const XcdBarrier& b) {
;     ...
;         const unsigned old = xb_add(&bar[XB_XSUB(b.x)], 1u);
;         const unsigned gen = old / nloc;
;         if (old + 1u == (gen + 1u) * nloc) {
;             __builtin_amdgcn_fence(__ATOMIC_RELEASE, "agent");
;             asm volatile("s_waitcnt vmcnt(0)" ::: "memory");
;             const unsigned og = xb_add(&bar[XB_TOP], 1u);
;             const unsigned tg = og / nx;
;             if (og + 1u == (tg + 1u) * nx) xb_add(&bar[XB_TOPGEN], 1u);
;             else XB_SPIN(xb_ld(&bar[XB_TOPGEN]) == tg, bar);
.LBB0_567:
	s_or_b64 exec, exec, s[42:43]
	v_cvt_f32_u32_e32 v5, v2
	s_waitcnt vmcnt(0)
	v_readfirstlane_b32 s0, v4
	s_add_u32 s42, s70, 0x4500
	s_addc_u32 s43, s71, 0
	v_rcp_iflag_f32_e32 v5, v5
	v_add_u32_e32 v3, s0, v3
	v_add_u32_e32 v6, 1, v3
	s_mov_b64 s[44:45], 0
	v_mul_f32_e32 v4, 0x4f7ffffe, v5
	v_cvt_u32_f32_e32 v4, v4
	v_sub_u32_e32 v5, 0, v2
	v_mul_lo_u32 v5, v5, v4
	v_mul_hi_u32 v5, v4, v5
	v_add_u32_e32 v4, v4, v5
	v_mul_hi_u32 v4, v3, v4
	v_mul_lo_u32 v5, v4, v2
	v_sub_u32_e32 v3, v3, v5
	v_add_u32_e32 v7, 1, v4
	v_cmp_ge_u32_e32 vcc, v3, v2
	v_sub_u32_e32 v5, v3, v2
	s_nop 0
	v_cndmask_b32_e32 v4, v4, v7, vcc
	v_cndmask_b32_e32 v3, v3, v5, vcc
	v_add_u32_e32 v5, 1, v4
	v_cmp_ge_u32_e32 vcc, v3, v2
	s_nop 1
	v_cndmask_b32_e32 v4, v4, v5, vcc
	v_mul_lo_u32 v3, v2, v4
	v_add_u32_e32 v2, v3, v2
	v_cmp_ne_u32_e32 vcc, v6, v2
	v_mov_b32_e32 v6, v2
	v_mov_b64_e32 v[2:3], s[42:43]
	s_and_saveexec_b64 s[40:41], vcc
	s_cbranch_execz .LBB0_579
	v_mov_b32_e32 v2, 0
	global_load_dword v3, v2, s[42:43] offset:-256 sc1
	s_mov_b64 s[50:51], 0
	s_waitcnt vmcnt(0)
	v_cmp_lt_u32_e32 vcc, v3, v6
	s_and_saveexec_b64 s[46:47], vcc
	s_cbranch_execz .LBB0_578
	s_add_u32 s44, s70, 0x1200
	s_addc_u32 s45, s71, 0
	s_mov_b32 s0, 1
	s_branch .LBB0_571

; __device__ __forceinline__ unsigned xb_ld(unsigned* p)              { return __hip_atomic_load(p, __ATOMIC_RELAXED, __HIP_MEMORY_SCOPE_AGENT); }
; __device__ __forceinline__ unsigned xb_add(unsigned* p, unsigned v) { return __hip_atomic_fetch_add(p, v, __ATOMIC_RELAXED, __HIP_MEMORY_SCOPE_AGENT); }
; #define XB_SPIN(cond, bar) do { unsigned _sp = 0; while (cond) { __builtin_amdgcn_s_sleep(1); \
;     if ((++_sp & 255u) == 0u) { if (xb_ld(&(bar)[XB_TMO])) break; if (_sp > XB_SPIN_CAP) { atomicAdd(&(bar)[XB_TMO], 1u); break; } } } } while (0)
; __device__ __forceinline__ void xcd_barrier(const XcdBarrier& b) {
;     ...
;             xb_add(&bar[XB_XGEN(b.x)], 1u);
;             __builtin_amdgcn_fence(__ATOMIC_ACQUIRE, "agent");
;         } else {
;             XB_SPIN(xb_ld(&bar[XB_XGEN(b.x)]) == gen, bar);
;             __builtin_amdgcn_fence(__ATOMIC_ACQUIRE, "agent");
.LBB0_581:
	s_or_b64 exec, exec, s[40:41]
	s_mov_b64 s[42:43], exec
	v_mbcnt_lo_u32_b32 v2, s42, 0
	v_mbcnt_hi_u32_b32 v2, s43, v2
	v_cmp_eq_u32_e32 vcc, 0, v2
	s_and_saveexec_b64 s[40:41], vcc
	s_cbranch_execz .LBB0_583
	s_bcnt1_i32_b64 s0, s[42:43]
	v_mov_b32_e32 v2, 0x2000
	v_mov_b32_e32 v3, s0
.LBB0_583:
	s_or_b64 exec, exec, s[40:41]
	s_waitcnt vmcnt(0)
	buffer_inv sc1

; __device__ __forceinline__ unsigned xb_ld(unsigned* p)              { return __hip_atomic_load(p, __ATOMIC_RELAXED, __HIP_MEMORY_SCOPE_AGENT); }
; __device__ __forceinline__ unsigned xb_add(unsigned* p, unsigned v) { return __hip_atomic_fetch_add(p, v, __ATOMIC_RELAXED, __HIP_MEMORY_SCOPE_AGENT); }
; #define XB_SPIN(cond, bar) do { unsigned _sp = 0; while (cond) { __builtin_amdgcn_s_sleep(1); \
;     if ((++_sp & 255u) == 0u) { if (xb_ld(&(bar)[XB_TMO])) break; if (_sp > XB_SPIN_CAP) { atomicAdd(&(bar)[XB_TMO], 1u); break; } } } } while (0)
; __device__ __forceinline__ void xcd_barrier(const XcdBarrier& b) {
;     ...
;             xb_add(&bar[XB_XGEN(b.x)], 1u);
;             __builtin_amdgcn_fence(__ATOMIC_ACQUIRE, "agent");
;         } else {
;             XB_SPIN(xb_ld(&bar[XB_XGEN(b.x)]) == gen, bar);
;             __builtin_amdgcn_fence(__ATOMIC_ACQUIRE, "agent");
.LBB0_650:
	s_or_b64 exec, exec, s[40:41]
	s_mov_b64 s[42:43], exec
	v_mbcnt_lo_u32_b32 v2, s42, 0
	v_mbcnt_hi_u32_b32 v2, s43, v2
	v_cmp_eq_u32_e32 vcc, 0, v2
	s_and_saveexec_b64 s[40:41], vcc
	s_cbranch_execz .LBB0_652
	s_bcnt1_i32_b64 s0, s[42:43]
	v_mov_b32_e32 v2, 0x2000
	v_mov_b32_e32 v3, s0
.LBB0_652:
	s_or_b64 exec, exec, s[40:41]
	s_waitcnt vmcnt(0)
	buffer_inv sc1

; __device__ __forceinline__ unsigned xb_ld(unsigned* p)              { return __hip_atomic_load(p, __ATOMIC_RELAXED, __HIP_MEMORY_SCOPE_AGENT); }
; __device__ __forceinline__ unsigned xb_add(unsigned* p, unsigned v) { return __hip_atomic_fetch_add(p, v, __ATOMIC_RELAXED, __HIP_MEMORY_SCOPE_AGENT); }
; #define XB_SPIN(cond, bar) do { unsigned _sp = 0; while (cond) { __builtin_amdgcn_s_sleep(1); \
;     if ((++_sp & 255u) == 0u) { if (xb_ld(&(bar)[XB_TMO])) break; if (_sp > XB_SPIN_CAP) { atomicAdd(&(bar)[XB_TMO], 1u); break; } } } } while (0)
; __device__ __forceinline__ void xcd_barrier(const XcdBarrier& b) {
;     ...
;             xb_add(&bar[XB_XGEN(b.x)], 1u);
;             __builtin_amdgcn_fence(__ATOMIC_ACQUIRE, "agent");
;         } else {
;             XB_SPIN(xb_ld(&bar[XB_XGEN(b.x)]) == gen, bar);
;             __builtin_amdgcn_fence(__ATOMIC_ACQUIRE, "agent");
.LBB0_723:
	s_or_b64 exec, exec, s[40:41]
	s_mov_b64 s[42:43], exec
	v_mbcnt_lo_u32_b32 v2, s42, 0
	v_mbcnt_hi_u32_b32 v2, s43, v2
	v_cmp_eq_u32_e32 vcc, 0, v2
	s_and_saveexec_b64 s[40:41], vcc
	s_cbranch_execz .LBB0_725
	s_bcnt1_i32_b64 s0, s[42:43]
	v_mov_b32_e32 v2, 0x2000
	v_mov_b32_e32 v3, s0
.LBB0_725:
	s_or_b64 exec, exec, s[40:41]
	s_waitcnt vmcnt(0)
	buffer_inv sc1

; __device__ __forceinline__ unsigned xb_ld(unsigned* p)              { return __hip_atomic_load(p, __ATOMIC_RELAXED, __HIP_MEMORY_SCOPE_AGENT); }
; __device__ __forceinline__ unsigned xb_add(unsigned* p, unsigned v) { return __hip_atomic_fetch_add(p, v, __ATOMIC_RELAXED, __HIP_MEMORY_SCOPE_AGENT); }
; #define XB_SPIN(cond, bar) do { unsigned _sp = 0; while (cond) { __builtin_amdgcn_s_sleep(1); \
;     if ((++_sp & 255u) == 0u) { if (xb_ld(&(bar)[XB_TMO])) break; if (_sp > XB_SPIN_CAP) { atomicAdd(&(bar)[XB_TMO], 1u); break; } } } } while (0)
; __device__ __forceinline__ void xcd_barrier(const XcdBarrier& b) {
;     ...
;         const unsigned old = xb_add(&bar[XB_XSUB(b.x)], 1u);
;         const unsigned gen = old / nloc;
;         if (old + 1u == (gen + 1u) * nloc) {
;             __builtin_amdgcn_fence(__ATOMIC_RELEASE, "agent");
;             asm volatile("s_waitcnt vmcnt(0)" ::: "memory");
;             const unsigned og = xb_add(&bar[XB_TOP], 1u);
;             const unsigned tg = og / nx;
;             if (og + 1u == (tg + 1u) * nx) xb_add(&bar[XB_TOPGEN], 1u);
;             else XB_SPIN(xb_ld(&bar[XB_TOPGEN]) == tg, bar);
.LBB0_765:
	s_or_b64 exec, exec, s[42:43]
	v_cvt_f32_u32_e32 v5, v2
	s_waitcnt vmcnt(0)
	v_readfirstlane_b32 s0, v4
	s_add_u32 s42, s70, 0x4500
	s_addc_u32 s43, s71, 0
	v_rcp_iflag_f32_e32 v5, v5
	v_add_u32_e32 v3, s0, v3
	v_add_u32_e32 v6, 1, v3
	s_mov_b64 s[44:45], 0
	v_mul_f32_e32 v4, 0x4f7ffffe, v5
	v_cvt_u32_f32_e32 v4, v4
	v_sub_u32_e32 v5, 0, v2
	v_mul_lo_u32 v5, v5, v4
	v_mul_hi_u32 v5, v4, v5
	v_add_u32_e32 v4, v4, v5
	v_mul_hi_u32 v4, v3, v4
	v_mul_lo_u32 v5, v4, v2
	v_sub_u32_e32 v3, v3, v5
	v_add_u32_e32 v7, 1, v4
	v_cmp_ge_u32_e32 vcc, v3, v2
	v_sub_u32_e32 v5, v3, v2
	s_nop 0
	v_cndmask_b32_e32 v4, v4, v7, vcc
	v_cndmask_b32_e32 v3, v3, v5, vcc
	v_add_u32_e32 v5, 1, v4
	v_cmp_ge_u32_e32 vcc, v3, v2
	s_nop 1
	v_cndmask_b32_e32 v4, v4, v5, vcc
	v_mul_lo_u32 v3, v2, v4
	v_add_u32_e32 v2, v3, v2
	v_cmp_ne_u32_e32 vcc, v6, v2
	v_mov_b32_e32 v6, v2
	v_mov_b64_e32 v[2:3], s[42:43]
	s_and_saveexec_b64 s[40:41], vcc
	s_cbranch_execz .LBB0_777
	v_mov_b32_e32 v2, 0
	global_load_dword v3, v2, s[42:43] offset:-256 sc1
	s_mov_b64 s[48:49], 0
	s_waitcnt vmcnt(0)
	v_cmp_lt_u32_e32 vcc, v3, v6
	s_and_saveexec_b64 s[46:47], vcc
	s_cbranch_execz .LBB0_776
	s_add_u32 s44, s70, 0x1200
	s_addc_u32 s45, s71, 0
	s_mov_b32 s0, 1
	s_branch .LBB0_769

; __device__ __forceinline__ unsigned xb_ld(unsigned* p)              { return __hip_atomic_load(p, __ATOMIC_RELAXED, __HIP_MEMORY_SCOPE_AGENT); }
; __device__ __forceinline__ unsigned xb_add(unsigned* p, unsigned v) { return __hip_atomic_fetch_add(p, v, __ATOMIC_RELAXED, __HIP_MEMORY_SCOPE_AGENT); }
; #define XB_SPIN(cond, bar) do { unsigned _sp = 0; while (cond) { __builtin_amdgcn_s_sleep(1); \
;     if ((++_sp & 255u) == 0u) { if (xb_ld(&(bar)[XB_TMO])) break; if (_sp > XB_SPIN_CAP) { atomicAdd(&(bar)[XB_TMO], 1u); break; } } } } while (0)
; __device__ __forceinline__ void xcd_barrier(const XcdBarrier& b) {
;     ...
;             xb_add(&bar[XB_XGEN(b.x)], 1u);
;             __builtin_amdgcn_fence(__ATOMIC_ACQUIRE, "agent");
;         } else {
;             XB_SPIN(xb_ld(&bar[XB_XGEN(b.x)]) == gen, bar);
;             __builtin_amdgcn_fence(__ATOMIC_ACQUIRE, "agent");
.LBB0_779:
	s_or_b64 exec, exec, s[40:41]
	s_mov_b64 s[42:43], exec
	v_mbcnt_lo_u32_b32 v2, s42, 0
	v_mbcnt_hi_u32_b32 v2, s43, v2
	v_cmp_eq_u32_e32 vcc, 0, v2
	s_and_saveexec_b64 s[40:41], vcc
	s_cbranch_execz .LBB0_781
	s_bcnt1_i32_b64 s0, s[42:43]
	v_mov_b32_e32 v2, 0x2000
	v_mov_b32_e32 v3, s0
.LBB0_781:
	s_or_b64 exec, exec, s[40:41]
	s_waitcnt vmcnt(0)
	buffer_inv sc1

; __device__ __forceinline__ unsigned xb_ld(unsigned* p)              { return __hip_atomic_load(p, __ATOMIC_RELAXED, __HIP_MEMORY_SCOPE_AGENT); }
; __device__ __forceinline__ unsigned xb_add(unsigned* p, unsigned v) { return __hip_atomic_fetch_add(p, v, __ATOMIC_RELAXED, __HIP_MEMORY_SCOPE_AGENT); }
; #define XB_SPIN(cond, bar) do { unsigned _sp = 0; while (cond) { __builtin_amdgcn_s_sleep(1); \
;     if ((++_sp & 255u) == 0u) { if (xb_ld(&(bar)[XB_TMO])) break; if (_sp > XB_SPIN_CAP) { atomicAdd(&(bar)[XB_TMO], 1u); break; } } } } while (0)
; __device__ __forceinline__ void xcd_barrier(const XcdBarrier& b) {
;     ...
;         const unsigned old = xb_add(&bar[XB_XSUB(b.x)], 1u);
;         const unsigned gen = old / nloc;
;         if (old + 1u == (gen + 1u) * nloc) {
;             __builtin_amdgcn_fence(__ATOMIC_RELEASE, "agent");
;             asm volatile("s_waitcnt vmcnt(0)" ::: "memory");
;             const unsigned og = xb_add(&bar[XB_TOP], 1u);
;             const unsigned tg = og / nx;
;             if (og + 1u == (tg + 1u) * nx) xb_add(&bar[XB_TOPGEN], 1u);
;             else XB_SPIN(xb_ld(&bar[XB_TOPGEN]) == tg, bar);
.LBB0_856:
	s_or_b64 exec, exec, s[38:39]
	v_cvt_f32_u32_e32 v5, v2
	s_waitcnt vmcnt(0)
	v_readfirstlane_b32 s0, v4
	s_add_u32 s38, s70, 0x4500
	s_addc_u32 s39, s71, 0
	v_rcp_iflag_f32_e32 v5, v5
	v_add_u32_e32 v3, s0, v3
	v_add_u32_e32 v6, 1, v3
	s_mov_b64 s[40:41], 0
	v_mul_f32_e32 v4, 0x4f7ffffe, v5
	v_cvt_u32_f32_e32 v4, v4
	v_sub_u32_e32 v5, 0, v2
	v_mul_lo_u32 v5, v5, v4
	v_mul_hi_u32 v5, v4, v5
	v_add_u32_e32 v4, v4, v5
	v_mul_hi_u32 v4, v3, v4
	v_mul_lo_u32 v5, v4, v2
	v_sub_u32_e32 v3, v3, v5
	v_add_u32_e32 v7, 1, v4
	v_cmp_ge_u32_e32 vcc, v3, v2
	v_sub_u32_e32 v5, v3, v2
	s_nop 0
	v_cndmask_b32_e32 v4, v4, v7, vcc
	v_cndmask_b32_e32 v3, v3, v5, vcc
	v_add_u32_e32 v5, 1, v4
	v_cmp_ge_u32_e32 vcc, v3, v2
	s_nop 1
	v_cndmask_b32_e32 v4, v4, v5, vcc
	v_mul_lo_u32 v3, v2, v4
	v_add_u32_e32 v2, v3, v2
	v_cmp_ne_u32_e32 vcc, v6, v2
	v_mov_b32_e32 v6, v2
	v_mov_b64_e32 v[2:3], s[38:39]
	s_and_saveexec_b64 s[22:23], vcc
	s_cbranch_execz .LBB0_868
	v_mov_b32_e32 v2, 0
	global_load_dword v3, v2, s[38:39] offset:-256 sc1
	s_mov_b64 s[44:45], 0
	s_waitcnt vmcnt(0)
	v_cmp_lt_u32_e32 vcc, v3, v6
	s_and_saveexec_b64 s[42:43], vcc
	s_cbranch_execz .LBB0_867
	s_add_u32 s40, s70, 0x1200
	s_addc_u32 s41, s71, 0
	s_mov_b32 s0, 1
	s_branch .LBB0_860

; __device__ __forceinline__ unsigned xb_ld(unsigned* p)              { return __hip_atomic_load(p, __ATOMIC_RELAXED, __HIP_MEMORY_SCOPE_AGENT); }
; __device__ __forceinline__ unsigned xb_add(unsigned* p, unsigned v) { return __hip_atomic_fetch_add(p, v, __ATOMIC_RELAXED, __HIP_MEMORY_SCOPE_AGENT); }
; #define XB_SPIN(cond, bar) do { unsigned _sp = 0; while (cond) { __builtin_amdgcn_s_sleep(1); \
;     if ((++_sp & 255u) == 0u) { if (xb_ld(&(bar)[XB_TMO])) break; if (_sp > XB_SPIN_CAP) { atomicAdd(&(bar)[XB_TMO], 1u); break; } } } } while (0)
; __device__ __forceinline__ void xcd_barrier(const XcdBarrier& b) {
;     ...
;             xb_add(&bar[XB_XGEN(b.x)], 1u);
;             __builtin_amdgcn_fence(__ATOMIC_ACQUIRE, "agent");
;         } else {
;             XB_SPIN(xb_ld(&bar[XB_XGEN(b.x)]) == gen, bar);
;             __builtin_amdgcn_fence(__ATOMIC_ACQUIRE, "agent");
.LBB0_870:
	s_or_b64 exec, exec, s[22:23]
	s_mov_b64 s[38:39], exec
	v_mbcnt_lo_u32_b32 v2, s38, 0
	v_mbcnt_hi_u32_b32 v2, s39, v2
	v_cmp_eq_u32_e32 vcc, 0, v2
	s_and_saveexec_b64 s[22:23], vcc
	s_cbranch_execz .LBB0_872
	s_bcnt1_i32_b64 s0, s[38:39]
	v_mov_b32_e32 v2, 0x2000
	v_mov_b32_e32 v3, s0
.LBB0_872:
	s_or_b64 exec, exec, s[22:23]
	s_waitcnt vmcnt(0)
	buffer_inv sc1

; __device__ __forceinline__ unsigned xb_ld(unsigned* p)              { return __hip_atomic_load(p, __ATOMIC_RELAXED, __HIP_MEMORY_SCOPE_AGENT); }
; __device__ __forceinline__ unsigned xb_add(unsigned* p, unsigned v) { return __hip_atomic_fetch_add(p, v, __ATOMIC_RELAXED, __HIP_MEMORY_SCOPE_AGENT); }
; #define XB_SPIN(cond, bar) do { unsigned _sp = 0; while (cond) { __builtin_amdgcn_s_sleep(1); \
;     if ((++_sp & 255u) == 0u) { if (xb_ld(&(bar)[XB_TMO])) break; if (_sp > XB_SPIN_CAP) { atomicAdd(&(bar)[XB_TMO], 1u); break; } } } } while (0)
; __device__ __forceinline__ void xcd_barrier(const XcdBarrier& b) {
;     ...
;         const unsigned old = xb_add(&bar[XB_XSUB(b.x)], 1u);
;         const unsigned gen = old / nloc;
;         if (old + 1u == (gen + 1u) * nloc) {
;             __builtin_amdgcn_fence(__ATOMIC_RELEASE, "agent");
;             asm volatile("s_waitcnt vmcnt(0)" ::: "memory");
;             const unsigned og = xb_add(&bar[XB_TOP], 1u);
;             const unsigned tg = og / nx;
;             if (og + 1u == (tg + 1u) * nx) xb_add(&bar[XB_TOPGEN], 1u);
;             else XB_SPIN(xb_ld(&bar[XB_TOPGEN]) == tg, bar);
.LBB0_914:
	s_or_b64 exec, exec, s[12:13]
	v_cvt_f32_u32_e32 v5, v2
	s_waitcnt vmcnt(0)
	v_readfirstlane_b32 s0, v4
	s_add_u32 s12, s70, 0x4500
	s_addc_u32 s13, s71, 0
	v_rcp_iflag_f32_e32 v5, v5
	v_add_u32_e32 v3, s0, v3
	v_add_u32_e32 v6, 1, v3
	s_mov_b64 s[14:15], 0
	v_mul_f32_e32 v4, 0x4f7ffffe, v5
	v_cvt_u32_f32_e32 v4, v4
	v_sub_u32_e32 v5, 0, v2
	v_mul_lo_u32 v5, v5, v4
	v_mul_hi_u32 v5, v4, v5
	v_add_u32_e32 v4, v4, v5
	v_mul_hi_u32 v4, v3, v4
	v_mul_lo_u32 v5, v4, v2
	v_sub_u32_e32 v3, v3, v5
	v_add_u32_e32 v7, 1, v4
	v_cmp_ge_u32_e32 vcc, v3, v2
	v_sub_u32_e32 v5, v3, v2
	s_nop 0
	v_cndmask_b32_e32 v4, v4, v7, vcc
	v_cndmask_b32_e32 v3, v3, v5, vcc
	v_add_u32_e32 v5, 1, v4
	v_cmp_ge_u32_e32 vcc, v3, v2
	s_nop 1
	v_cndmask_b32_e32 v4, v4, v5, vcc
	v_mul_lo_u32 v3, v2, v4
	v_add_u32_e32 v2, v3, v2
	v_cmp_ne_u32_e32 vcc, v6, v2
	v_mov_b32_e32 v6, v2
	v_mov_b64_e32 v[2:3], s[12:13]
	s_and_saveexec_b64 s[8:9], vcc
	s_cbranch_execz .LBB0_926
	v_mov_b32_e32 v2, 0
	global_load_dword v3, v2, s[12:13] offset:-256 sc1
	s_mov_b64 s[30:31], 0
	s_waitcnt vmcnt(0)
	v_cmp_lt_u32_e32 vcc, v3, v6
	s_and_saveexec_b64 s[22:23], vcc
	s_cbranch_execz .LBB0_925
	s_add_u32 s14, s70, 0x1200
	s_addc_u32 s15, s71, 0
	s_mov_b32 s0, 1
	s_branch .LBB0_918

; __device__ __forceinline__ unsigned xb_ld(unsigned* p)              { return __hip_atomic_load(p, __ATOMIC_RELAXED, __HIP_MEMORY_SCOPE_AGENT); }
; __device__ __forceinline__ unsigned xb_add(unsigned* p, unsigned v) { return __hip_atomic_fetch_add(p, v, __ATOMIC_RELAXED, __HIP_MEMORY_SCOPE_AGENT); }
; #define XB_SPIN(cond, bar) do { unsigned _sp = 0; while (cond) { __builtin_amdgcn_s_sleep(1); \
;     if ((++_sp & 255u) == 0u) { if (xb_ld(&(bar)[XB_TMO])) break; if (_sp > XB_SPIN_CAP) { atomicAdd(&(bar)[XB_TMO], 1u); break; } } } } while (0)
; __device__ __forceinline__ void xcd_barrier(const XcdBarrier& b) {
;     ...
;             xb_add(&bar[XB_XGEN(b.x)], 1u);
;             __builtin_amdgcn_fence(__ATOMIC_ACQUIRE, "agent");
;         } else {
;             XB_SPIN(xb_ld(&bar[XB_XGEN(b.x)]) == gen, bar);
;             __builtin_amdgcn_fence(__ATOMIC_ACQUIRE, "agent");
.LBB0_928:
	s_or_b64 exec, exec, s[8:9]
	s_mov_b64 s[12:13], exec
	v_mbcnt_lo_u32_b32 v2, s12, 0
	v_mbcnt_hi_u32_b32 v2, s13, v2
	v_cmp_eq_u32_e32 vcc, 0, v2
	s_and_saveexec_b64 s[8:9], vcc
	s_cbranch_execz .LBB0_930
	s_bcnt1_i32_b64 s0, s[12:13]
	v_mov_b32_e32 v2, 0x2000
	v_mov_b32_e32 v3, s0
.LBB0_930:
	s_or_b64 exec, exec, s[8:9]
	s_waitcnt vmcnt(0)
	buffer_inv sc1

; __device__ __forceinline__ unsigned xb_ld(unsigned* p)              { return __hip_atomic_load(p, __ATOMIC_RELAXED, __HIP_MEMORY_SCOPE_AGENT); }
; __device__ __forceinline__ unsigned xb_add(unsigned* p, unsigned v) { return __hip_atomic_fetch_add(p, v, __ATOMIC_RELAXED, __HIP_MEMORY_SCOPE_AGENT); }
; #define XB_SPIN(cond, bar) do { unsigned _sp = 0; while (cond) { __builtin_amdgcn_s_sleep(1); \
;     if ((++_sp & 255u) == 0u) { if (xb_ld(&(bar)[XB_TMO])) break; if (_sp > XB_SPIN_CAP) { atomicAdd(&(bar)[XB_TMO], 1u); break; } } } } while (0)
; __device__ __forceinline__ void xcd_barrier(const XcdBarrier& b) {
;     ...
;         const unsigned old = xb_add(&bar[XB_XSUB(b.x)], 1u);
;         const unsigned gen = old / nloc;
;         if (old + 1u == (gen + 1u) * nloc) {
;             __builtin_amdgcn_fence(__ATOMIC_RELEASE, "agent");
;             asm volatile("s_waitcnt vmcnt(0)" ::: "memory");
;             const unsigned og = xb_add(&bar[XB_TOP], 1u);
;             const unsigned tg = og / nx;
;             if (og + 1u == (tg + 1u) * nx) xb_add(&bar[XB_TOPGEN], 1u);
;             else XB_SPIN(xb_ld(&bar[XB_TOPGEN]) == tg, bar);
.LBB0_1002:
	s_or_b64 exec, exec, s[22:23]
	v_cvt_f32_u32_e32 v5, v2
	s_waitcnt vmcnt(0)
	v_readfirstlane_b32 s0, v4
	s_add_u32 s22, s70, 0x4500
	s_addc_u32 s23, s71, 0
	v_rcp_iflag_f32_e32 v5, v5
	v_add_u32_e32 v3, s0, v3
	v_add_u32_e32 v6, 1, v3
	s_mov_b64 s[30:31], 0
	v_mul_f32_e32 v4, 0x4f7ffffe, v5
	v_cvt_u32_f32_e32 v4, v4
	v_sub_u32_e32 v5, 0, v2
	v_mul_lo_u32 v5, v5, v4
	v_mul_hi_u32 v5, v4, v5
	v_add_u32_e32 v4, v4, v5
	v_mul_hi_u32 v4, v3, v4
	v_mul_lo_u32 v5, v4, v2
	v_sub_u32_e32 v3, v3, v5
	v_add_u32_e32 v7, 1, v4
	v_cmp_ge_u32_e32 vcc, v3, v2
	v_sub_u32_e32 v5, v3, v2
	s_nop 0
	v_cndmask_b32_e32 v4, v4, v7, vcc
	v_cndmask_b32_e32 v3, v3, v5, vcc
	v_add_u32_e32 v5, 1, v4
	v_cmp_ge_u32_e32 vcc, v3, v2
	s_nop 1
	v_cndmask_b32_e32 v4, v4, v5, vcc
	v_mul_lo_u32 v3, v2, v4
	v_add_u32_e32 v2, v3, v2
	v_cmp_ne_u32_e32 vcc, v6, v2
	v_mov_b32_e32 v6, v2
	v_mov_b64_e32 v[2:3], s[22:23]
	s_and_saveexec_b64 s[14:15], vcc
	s_cbranch_execz .LBB0_1014
	v_mov_b32_e32 v2, 0
	global_load_dword v3, v2, s[22:23] offset:-256 sc1
	s_mov_b64 s[40:41], 0
	s_waitcnt vmcnt(0)
	v_cmp_lt_u32_e32 vcc, v3, v6
	s_and_saveexec_b64 s[38:39], vcc
	s_cbranch_execz .LBB0_1013
	s_add_u32 s30, s70, 0x1200
	s_addc_u32 s31, s71, 0
	s_mov_b32 s0, 1
	s_branch .LBB0_1006

; __device__ __forceinline__ unsigned xb_ld(unsigned* p)              { return __hip_atomic_load(p, __ATOMIC_RELAXED, __HIP_MEMORY_SCOPE_AGENT); }
; __device__ __forceinline__ unsigned xb_add(unsigned* p, unsigned v) { return __hip_atomic_fetch_add(p, v, __ATOMIC_RELAXED, __HIP_MEMORY_SCOPE_AGENT); }
; #define XB_SPIN(cond, bar) do { unsigned _sp = 0; while (cond) { __builtin_amdgcn_s_sleep(1); \
;     if ((++_sp & 255u) == 0u) { if (xb_ld(&(bar)[XB_TMO])) break; if (_sp > XB_SPIN_CAP) { atomicAdd(&(bar)[XB_TMO], 1u); break; } } } } while (0)
; __device__ __forceinline__ void xcd_barrier(const XcdBarrier& b) {
;     ...
;             xb_add(&bar[XB_XGEN(b.x)], 1u);
;             __builtin_amdgcn_fence(__ATOMIC_ACQUIRE, "agent");
;         } else {
;             XB_SPIN(xb_ld(&bar[XB_XGEN(b.x)]) == gen, bar);
;             __builtin_amdgcn_fence(__ATOMIC_ACQUIRE, "agent");
.LBB0_1016:
	s_or_b64 exec, exec, s[14:15]
	s_mov_b64 s[22:23], exec
	v_mbcnt_lo_u32_b32 v2, s22, 0
	v_mbcnt_hi_u32_b32 v2, s23, v2
	v_cmp_eq_u32_e32 vcc, 0, v2
	s_and_saveexec_b64 s[14:15], vcc
	s_cbranch_execz .LBB0_1018
	s_bcnt1_i32_b64 s0, s[22:23]
	v_mov_b32_e32 v2, 0x2000
	v_mov_b32_e32 v3, s0
.LBB0_1018:
	s_or_b64 exec, exec, s[14:15]
	s_waitcnt vmcnt(0)
	buffer_inv sc1

; __device__ __forceinline__ unsigned xb_ld(unsigned* p)              { return __hip_atomic_load(p, __ATOMIC_RELAXED, __HIP_MEMORY_SCOPE_AGENT); }
; __device__ __forceinline__ unsigned xb_add(unsigned* p, unsigned v) { return __hip_atomic_fetch_add(p, v, __ATOMIC_RELAXED, __HIP_MEMORY_SCOPE_AGENT); }
; #define XB_SPIN(cond, bar) do { unsigned _sp = 0; while (cond) { __builtin_amdgcn_s_sleep(1); \
;     if ((++_sp & 255u) == 0u) { if (xb_ld(&(bar)[XB_TMO])) break; if (_sp > XB_SPIN_CAP) { atomicAdd(&(bar)[XB_TMO], 1u); break; } } } } while (0)
; __device__ __forceinline__ void xcd_barrier(const XcdBarrier& b) {
;     ...
;         const unsigned old = xb_add(&bar[XB_XSUB(b.x)], 1u);
;         const unsigned gen = old / nloc;
;         if (old + 1u == (gen + 1u) * nloc) {
;             __builtin_amdgcn_fence(__ATOMIC_RELEASE, "agent");
;             asm volatile("s_waitcnt vmcnt(0)" ::: "memory");
;             const unsigned og = xb_add(&bar[XB_TOP], 1u);
;             const unsigned tg = og / nx;
;             if (og + 1u == (tg + 1u) * nx) xb_add(&bar[XB_TOPGEN], 1u);
;             else XB_SPIN(xb_ld(&bar[XB_TOPGEN]) == tg, bar);
.LBB0_1091:
	s_or_b64 exec, exec, s[12:13]
	v_cvt_f32_u32_e32 v5, v2
	s_waitcnt vmcnt(0)
	v_readfirstlane_b32 s10, v4
	s_add_u32 s12, s70, 0x4500
	s_addc_u32 s13, s71, 0
	v_rcp_iflag_f32_e32 v5, v5
	v_add_u32_e32 v3, s10, v3
	v_add_u32_e32 v6, 1, v3
	s_mov_b64 s[14:15], 0
	v_mul_f32_e32 v4, 0x4f7ffffe, v5
	v_cvt_u32_f32_e32 v4, v4
	v_sub_u32_e32 v5, 0, v2
	v_mul_lo_u32 v5, v5, v4
	v_mul_hi_u32 v5, v4, v5
	v_add_u32_e32 v4, v4, v5
	v_mul_hi_u32 v4, v3, v4
	v_mul_lo_u32 v5, v4, v2
	v_sub_u32_e32 v3, v3, v5
	v_add_u32_e32 v7, 1, v4
	v_cmp_ge_u32_e32 vcc, v3, v2
	v_sub_u32_e32 v5, v3, v2
	s_nop 0
	v_cndmask_b32_e32 v4, v4, v7, vcc
	v_cndmask_b32_e32 v3, v3, v5, vcc
	v_add_u32_e32 v5, 1, v4
	v_cmp_ge_u32_e32 vcc, v3, v2
	s_nop 1
	v_cndmask_b32_e32 v4, v4, v5, vcc
	v_mul_lo_u32 v3, v2, v4
	v_add_u32_e32 v2, v3, v2
	v_cmp_ne_u32_e32 vcc, v6, v2
	v_mov_b32_e32 v6, v2
	v_mov_b64_e32 v[2:3], s[12:13]
	s_and_saveexec_b64 s[10:11], vcc
	s_cbranch_execz .LBB0_1103
	v_mov_b32_e32 v2, 0
	global_load_dword v3, v2, s[12:13] offset:-256 sc1
	s_mov_b64 s[26:27], 0
	s_waitcnt vmcnt(0)
	v_cmp_lt_u32_e32 vcc, v3, v6
	s_and_saveexec_b64 s[22:23], vcc
	s_cbranch_execz .LBB0_1102
	s_add_u32 s14, s70, 0x1200
	s_addc_u32 s15, s71, 0
	s_mov_b32 s18, 1
	s_branch .LBB0_1095

; __device__ __forceinline__ unsigned xb_ld(unsigned* p)              { return __hip_atomic_load(p, __ATOMIC_RELAXED, __HIP_MEMORY_SCOPE_AGENT); }
; __device__ __forceinline__ unsigned xb_add(unsigned* p, unsigned v) { return __hip_atomic_fetch_add(p, v, __ATOMIC_RELAXED, __HIP_MEMORY_SCOPE_AGENT); }
; #define XB_SPIN(cond, bar) do { unsigned _sp = 0; while (cond) { __builtin_amdgcn_s_sleep(1); \
;     if ((++_sp & 255u) == 0u) { if (xb_ld(&(bar)[XB_TMO])) break; if (_sp > XB_SPIN_CAP) { atomicAdd(&(bar)[XB_TMO], 1u); break; } } } } while (0)
; __device__ __forceinline__ void xcd_barrier(const XcdBarrier& b) {
;     ...
;             xb_add(&bar[XB_XGEN(b.x)], 1u);
;             __builtin_amdgcn_fence(__ATOMIC_ACQUIRE, "agent");
;         } else {
;             XB_SPIN(xb_ld(&bar[XB_XGEN(b.x)]) == gen, bar);
;             __builtin_amdgcn_fence(__ATOMIC_ACQUIRE, "agent");
.LBB0_1105:
	s_or_b64 exec, exec, s[10:11]
	s_mov_b64 s[12:13], exec
	v_mbcnt_lo_u32_b32 v2, s12, 0
	v_mbcnt_hi_u32_b32 v2, s13, v2
	v_cmp_eq_u32_e32 vcc, 0, v2
	s_and_saveexec_b64 s[10:11], vcc
	s_cbranch_execz .LBB0_1107
	s_bcnt1_i32_b64 s12, s[12:13]
	v_mov_b32_e32 v2, 0x2000
	v_mov_b32_e32 v3, s12
.LBB0_1107:
	s_or_b64 exec, exec, s[10:11]
	s_waitcnt vmcnt(0)
	buffer_inv sc1

; __device__ __forceinline__ unsigned xb_ld(unsigned* p)              { return __hip_atomic_load(p, __ATOMIC_RELAXED, __HIP_MEMORY_SCOPE_AGENT); }
; __device__ __forceinline__ unsigned xb_add(unsigned* p, unsigned v) { return __hip_atomic_fetch_add(p, v, __ATOMIC_RELAXED, __HIP_MEMORY_SCOPE_AGENT); }
; #define XB_SPIN(cond, bar) do { unsigned _sp = 0; while (cond) { __builtin_amdgcn_s_sleep(1); \
;     if ((++_sp & 255u) == 0u) { if (xb_ld(&(bar)[XB_TMO])) break; if (_sp > XB_SPIN_CAP) { atomicAdd(&(bar)[XB_TMO], 1u); break; } } } } while (0)
; __device__ __forceinline__ void xcd_barrier(const XcdBarrier& b) {
;     ...
;         const unsigned old = xb_add(&bar[XB_XSUB(b.x)], 1u);
;         const unsigned gen = old / nloc;
;         if (old + 1u == (gen + 1u) * nloc) {
;             __builtin_amdgcn_fence(__ATOMIC_RELEASE, "agent");
;             asm volatile("s_waitcnt vmcnt(0)" ::: "memory");
;             const unsigned og = xb_add(&bar[XB_TOP], 1u);
;             const unsigned tg = og / nx;
;             if (og + 1u == (tg + 1u) * nx) xb_add(&bar[XB_TOPGEN], 1u);
;             else XB_SPIN(xb_ld(&bar[XB_TOPGEN]) == tg, bar);
.LBB0_1163:
	s_or_b64 exec, exec, s[12:13]
	v_cvt_f32_u32_e32 v5, v2
	s_waitcnt vmcnt(0)
	v_readfirstlane_b32 s10, v4
	s_add_u32 s12, s70, 0x4500
	s_addc_u32 s13, s71, 0
	v_rcp_iflag_f32_e32 v5, v5
	v_add_u32_e32 v3, s10, v3
	v_add_u32_e32 v6, 1, v3
	s_mov_b64 s[14:15], 0
	v_mul_f32_e32 v4, 0x4f7ffffe, v5
	v_cvt_u32_f32_e32 v4, v4
	v_sub_u32_e32 v5, 0, v2
	v_mul_lo_u32 v5, v5, v4
	v_mul_hi_u32 v5, v4, v5
	v_add_u32_e32 v4, v4, v5
	v_mul_hi_u32 v4, v3, v4
	v_mul_lo_u32 v5, v4, v2
	v_sub_u32_e32 v3, v3, v5
	v_add_u32_e32 v7, 1, v4
	v_cmp_ge_u32_e32 vcc, v3, v2
	v_sub_u32_e32 v5, v3, v2
	s_nop 0
	v_cndmask_b32_e32 v4, v4, v7, vcc
	v_cndmask_b32_e32 v3, v3, v5, vcc
	v_add_u32_e32 v5, 1, v4
	v_cmp_ge_u32_e32 vcc, v3, v2
	s_nop 1
	v_cndmask_b32_e32 v4, v4, v5, vcc
	v_mul_lo_u32 v3, v2, v4
	v_add_u32_e32 v2, v3, v2
	v_cmp_ne_u32_e32 vcc, v6, v2
	v_mov_b32_e32 v6, v2
	v_mov_b64_e32 v[2:3], s[12:13]
	s_and_saveexec_b64 s[10:11], vcc
	s_cbranch_execz .LBB0_1175
	v_mov_b32_e32 v2, 0
	global_load_dword v3, v2, s[12:13] offset:-256 sc1
	s_mov_b64 s[22:23], 0
	s_waitcnt vmcnt(0)
	v_cmp_lt_u32_e32 vcc, v3, v6
	s_and_saveexec_b64 s[16:17], vcc
	s_cbranch_execz .LBB0_1174
	s_add_u32 s14, s70, 0x1200
	s_addc_u32 s15, s71, 0
	s_mov_b32 s18, 1
	s_branch .LBB0_1167

; __device__ __forceinline__ unsigned xb_ld(unsigned* p)              { return __hip_atomic_load(p, __ATOMIC_RELAXED, __HIP_MEMORY_SCOPE_AGENT); }
; __device__ __forceinline__ unsigned xb_add(unsigned* p, unsigned v) { return __hip_atomic_fetch_add(p, v, __ATOMIC_RELAXED, __HIP_MEMORY_SCOPE_AGENT); }
; #define XB_SPIN(cond, bar) do { unsigned _sp = 0; while (cond) { __builtin_amdgcn_s_sleep(1); \
;     if ((++_sp & 255u) == 0u) { if (xb_ld(&(bar)[XB_TMO])) break; if (_sp > XB_SPIN_CAP) { atomicAdd(&(bar)[XB_TMO], 1u); break; } } } } while (0)
; __device__ __forceinline__ void xcd_barrier(const XcdBarrier& b) {
;     ...
;             xb_add(&bar[XB_XGEN(b.x)], 1u);
;             __builtin_amdgcn_fence(__ATOMIC_ACQUIRE, "agent");
;         } else {
;             XB_SPIN(xb_ld(&bar[XB_XGEN(b.x)]) == gen, bar);
;             __builtin_amdgcn_fence(__ATOMIC_ACQUIRE, "agent");
.LBB0_1177:
	s_or_b64 exec, exec, s[10:11]
	s_mov_b64 s[12:13], exec
	v_mbcnt_lo_u32_b32 v2, s12, 0
	v_mbcnt_hi_u32_b32 v2, s13, v2
	v_cmp_eq_u32_e32 vcc, 0, v2
	s_and_saveexec_b64 s[10:11], vcc
	s_cbranch_execz .LBB0_1179
	s_bcnt1_i32_b64 s12, s[12:13]
	v_mov_b32_e32 v2, 0x2000
	v_mov_b32_e32 v3, s12
.LBB0_1179:
	s_or_b64 exec, exec, s[10:11]
	s_waitcnt vmcnt(0)
	buffer_inv sc1

; __device__ __forceinline__ unsigned xb_ld(unsigned* p)              { return __hip_atomic_load(p, __ATOMIC_RELAXED, __HIP_MEMORY_SCOPE_AGENT); }
; __device__ __forceinline__ unsigned xb_add(unsigned* p, unsigned v) { return __hip_atomic_fetch_add(p, v, __ATOMIC_RELAXED, __HIP_MEMORY_SCOPE_AGENT); }
; #define XB_SPIN(cond, bar) do { unsigned _sp = 0; while (cond) { __builtin_amdgcn_s_sleep(1); \
;     if ((++_sp & 255u) == 0u) { if (xb_ld(&(bar)[XB_TMO])) break; if (_sp > XB_SPIN_CAP) { atomicAdd(&(bar)[XB_TMO], 1u); break; } } } } while (0)
; __device__ __forceinline__ void xcd_barrier(const XcdBarrier& b) {
;     ...
;         const unsigned old = xb_add(&bar[XB_XSUB(b.x)], 1u);
;         const unsigned gen = old / nloc;
;         if (old + 1u == (gen + 1u) * nloc) {
;             __builtin_amdgcn_fence(__ATOMIC_RELEASE, "agent");
;             asm volatile("s_waitcnt vmcnt(0)" ::: "memory");
;             const unsigned og = xb_add(&bar[XB_TOP], 1u);
;             const unsigned tg = og / nx;
;             if (og + 1u == (tg + 1u) * nx) xb_add(&bar[XB_TOPGEN], 1u);
;             else XB_SPIN(xb_ld(&bar[XB_TOPGEN]) == tg, bar);
.LBB0_1225:
	s_or_b64 exec, exec, s[14:15]
	v_cvt_f32_u32_e32 v4, v1
	s_waitcnt vmcnt(0)
	v_readfirstlane_b32 s12, v3
	s_add_u32 s14, s70, 0x4500
	s_addc_u32 s15, s71, 0
	v_rcp_iflag_f32_e32 v4, v4
	v_add_u32_e32 v2, s12, v2
	v_add_u32_e32 v5, 1, v2
	s_mov_b64 s[16:17], 0
	v_mul_f32_e32 v3, 0x4f7ffffe, v4
	v_cvt_u32_f32_e32 v3, v3
	v_sub_u32_e32 v4, 0, v1
	v_mul_lo_u32 v4, v4, v3
	v_mul_hi_u32 v4, v3, v4
	v_add_u32_e32 v3, v3, v4
	v_mul_hi_u32 v3, v2, v3
	v_mul_lo_u32 v4, v3, v1
	v_sub_u32_e32 v2, v2, v4
	v_add_u32_e32 v6, 1, v3
	v_cmp_ge_u32_e32 vcc, v2, v1
	v_sub_u32_e32 v4, v2, v1
	s_nop 0
	v_cndmask_b32_e32 v3, v3, v6, vcc
	v_cndmask_b32_e32 v2, v2, v4, vcc
	v_add_u32_e32 v4, 1, v3
	v_cmp_ge_u32_e32 vcc, v2, v1
	s_nop 1
	v_cndmask_b32_e32 v4, v3, v4, vcc
	v_mul_lo_u32 v2, v1, v4
	v_add_u32_e32 v1, v2, v1
	v_cmp_ne_u32_e32 vcc, v5, v1
	v_mov_b32_e32 v5, v1
	v_mov_b64_e32 v[2:3], s[14:15]
	s_and_saveexec_b64 s[12:13], vcc
	s_cbranch_execz .LBB0_1237
	v_mov_b32_e32 v1, 0
	global_load_dword v2, v1, s[14:15] offset:-256 sc1
	s_mov_b64 s[20:21], 0
	s_waitcnt vmcnt(0)
	v_cmp_lt_u32_e32 vcc, v2, v5
	s_and_saveexec_b64 s[18:19], vcc
	s_cbranch_execz .LBB0_1236
	s_add_u32 s16, s70, 0x1200
	s_addc_u32 s17, s71, 0
	s_mov_b32 s24, 1
	s_branch .LBB0_1229

; __device__ __forceinline__ unsigned xb_ld(unsigned* p)              { return __hip_atomic_load(p, __ATOMIC_RELAXED, __HIP_MEMORY_SCOPE_AGENT); }
; __device__ __forceinline__ unsigned xb_add(unsigned* p, unsigned v) { return __hip_atomic_fetch_add(p, v, __ATOMIC_RELAXED, __HIP_MEMORY_SCOPE_AGENT); }
; #define XB_SPIN(cond, bar) do { unsigned _sp = 0; while (cond) { __builtin_amdgcn_s_sleep(1); \
;     if ((++_sp & 255u) == 0u) { if (xb_ld(&(bar)[XB_TMO])) break; if (_sp > XB_SPIN_CAP) { atomicAdd(&(bar)[XB_TMO], 1u); break; } } } } while (0)
; __device__ __forceinline__ void xcd_barrier(const XcdBarrier& b) {
;     ...
;             xb_add(&bar[XB_XGEN(b.x)], 1u);
;             __builtin_amdgcn_fence(__ATOMIC_ACQUIRE, "agent");
;         } else {
;             XB_SPIN(xb_ld(&bar[XB_XGEN(b.x)]) == gen, bar);
;             __builtin_amdgcn_fence(__ATOMIC_ACQUIRE, "agent");
.LBB0_1239:
	s_or_b64 exec, exec, s[12:13]
	s_mov_b64 s[14:15], exec
	v_mbcnt_lo_u32_b32 v1, s14, 0
	v_mbcnt_hi_u32_b32 v1, s15, v1
	v_cmp_eq_u32_e32 vcc, 0, v1
	s_and_saveexec_b64 s[12:13], vcc
	s_cbranch_execz .LBB0_1241
	s_bcnt1_i32_b64 s14, s[14:15]
	v_mov_b32_e32 v1, 0x2000
	v_mov_b32_e32 v2, s14
.LBB0_1241:
	s_or_b64 exec, exec, s[12:13]
	s_waitcnt vmcnt(0)
	buffer_inv sc1

; __device__ __forceinline__ unsigned xb_ld(unsigned* p)              { return __hip_atomic_load(p, __ATOMIC_RELAXED, __HIP_MEMORY_SCOPE_AGENT); }
; __device__ __forceinline__ unsigned xb_add(unsigned* p, unsigned v) { return __hip_atomic_fetch_add(p, v, __ATOMIC_RELAXED, __HIP_MEMORY_SCOPE_AGENT); }
; #define XB_SPIN(cond, bar) do { unsigned _sp = 0; while (cond) { __builtin_amdgcn_s_sleep(1); \
;     if ((++_sp & 255u) == 0u) { if (xb_ld(&(bar)[XB_TMO])) break; if (_sp > XB_SPIN_CAP) { atomicAdd(&(bar)[XB_TMO], 1u); break; } } } } while (0)
; __device__ __forceinline__ void xcd_barrier(const XcdBarrier& b) {
;     ...
;         const unsigned old = xb_add(&bar[XB_XSUB(b.x)], 1u);
;         const unsigned gen = old / nloc;
;         if (old + 1u == (gen + 1u) * nloc) {
;             __builtin_amdgcn_fence(__ATOMIC_RELEASE, "agent");
;             asm volatile("s_waitcnt vmcnt(0)" ::: "memory");
;             const unsigned og = xb_add(&bar[XB_TOP], 1u);
;             const unsigned tg = og / nx;
;             if (og + 1u == (tg + 1u) * nx) xb_add(&bar[XB_TOPGEN], 1u);
;             else XB_SPIN(xb_ld(&bar[XB_TOPGEN]) == tg, bar);
.LBB0_1380:
	s_or_b64 exec, exec, s[16:17]
	v_cvt_f32_u32_e32 v4, v1
	s_waitcnt vmcnt(0)
	v_readfirstlane_b32 s14, v3
	s_add_u32 s16, s70, 0x4500
	s_addc_u32 s17, s71, 0
	v_rcp_iflag_f32_e32 v4, v4
	v_add_u32_e32 v2, s14, v2
	v_add_u32_e32 v5, 1, v2
	s_mov_b64 s[18:19], 0
	v_mul_f32_e32 v3, 0x4f7ffffe, v4
	v_cvt_u32_f32_e32 v3, v3
	v_sub_u32_e32 v4, 0, v1
	v_mul_lo_u32 v4, v4, v3
	v_mul_hi_u32 v4, v3, v4
	v_add_u32_e32 v3, v3, v4
	v_mul_hi_u32 v3, v2, v3
	v_mul_lo_u32 v4, v3, v1
	v_sub_u32_e32 v2, v2, v4
	v_add_u32_e32 v6, 1, v3
	v_cmp_ge_u32_e32 vcc, v2, v1
	v_sub_u32_e32 v4, v2, v1
	s_nop 0
	v_cndmask_b32_e32 v3, v3, v6, vcc
	v_cndmask_b32_e32 v2, v2, v4, vcc
	v_add_u32_e32 v4, 1, v3
	v_cmp_ge_u32_e32 vcc, v2, v1
	s_nop 1
	v_cndmask_b32_e32 v4, v3, v4, vcc
	v_mul_lo_u32 v2, v1, v4
	v_add_u32_e32 v1, v2, v1
	v_cmp_ne_u32_e32 vcc, v5, v1
	v_mov_b32_e32 v5, v1
	v_mov_b64_e32 v[2:3], s[16:17]
	s_and_saveexec_b64 s[14:15], vcc
	s_cbranch_execz .LBB0_1392
	v_mov_b32_e32 v1, 0
	global_load_dword v2, v1, s[16:17] offset:-256 sc1
	s_mov_b64 s[22:23], 0
	s_waitcnt vmcnt(0)
	v_cmp_lt_u32_e32 vcc, v2, v5
	s_and_saveexec_b64 s[20:21], vcc
	s_cbranch_execz .LBB0_1391
	s_add_u32 s18, s70, 0x1200
	s_addc_u32 s19, s71, 0
	s_mov_b32 s24, 1
	s_branch .LBB0_1384

; __device__ __forceinline__ unsigned xb_ld(unsigned* p)              { return __hip_atomic_load(p, __ATOMIC_RELAXED, __HIP_MEMORY_SCOPE_AGENT); }
; __device__ __forceinline__ unsigned xb_add(unsigned* p, unsigned v) { return __hip_atomic_fetch_add(p, v, __ATOMIC_RELAXED, __HIP_MEMORY_SCOPE_AGENT); }
; #define XB_SPIN(cond, bar) do { unsigned _sp = 0; while (cond) { __builtin_amdgcn_s_sleep(1); \
;     if ((++_sp & 255u) == 0u) { if (xb_ld(&(bar)[XB_TMO])) break; if (_sp > XB_SPIN_CAP) { atomicAdd(&(bar)[XB_TMO], 1u); break; } } } } while (0)
; __device__ __forceinline__ void xcd_barrier(const XcdBarrier& b) {
;     ...
;             xb_add(&bar[XB_XGEN(b.x)], 1u);
;             __builtin_amdgcn_fence(__ATOMIC_ACQUIRE, "agent");
;         } else {
;             XB_SPIN(xb_ld(&bar[XB_XGEN(b.x)]) == gen, bar);
;             __builtin_amdgcn_fence(__ATOMIC_ACQUIRE, "agent");
.LBB0_1394:
	s_or_b64 exec, exec, s[14:15]
	s_mov_b64 s[16:17], exec
	v_mbcnt_lo_u32_b32 v1, s16, 0
	v_mbcnt_hi_u32_b32 v1, s17, v1
	v_cmp_eq_u32_e32 vcc, 0, v1
	s_and_saveexec_b64 s[14:15], vcc
	s_cbranch_execz .LBB0_1396
	s_bcnt1_i32_b64 s16, s[16:17]
	v_mov_b32_e32 v1, 0x2000
	v_mov_b32_e32 v2, s16
.LBB0_1396:
	s_or_b64 exec, exec, s[14:15]
	s_waitcnt vmcnt(0)
	buffer_inv sc1

; __device__ __forceinline__ unsigned xb_ld(unsigned* p)              { return __hip_atomic_load(p, __ATOMIC_RELAXED, __HIP_MEMORY_SCOPE_AGENT); }
; __device__ __forceinline__ unsigned xb_add(unsigned* p, unsigned v) { return __hip_atomic_fetch_add(p, v, __ATOMIC_RELAXED, __HIP_MEMORY_SCOPE_AGENT); }
; #define XB_SPIN(cond, bar) do { unsigned _sp = 0; while (cond) { __builtin_amdgcn_s_sleep(1); \
;     if ((++_sp & 255u) == 0u) { if (xb_ld(&(bar)[XB_TMO])) break; if (_sp > XB_SPIN_CAP) { atomicAdd(&(bar)[XB_TMO], 1u); break; } } } } while (0)
; __device__ __forceinline__ void xcd_barrier(const XcdBarrier& b) {
;     ...
;         const unsigned old = xb_add(&bar[XB_XSUB(b.x)], 1u);
;         const unsigned gen = old / nloc;
;         if (old + 1u == (gen + 1u) * nloc) {
;             __builtin_amdgcn_fence(__ATOMIC_RELEASE, "agent");
;             asm volatile("s_waitcnt vmcnt(0)" ::: "memory");
;             const unsigned og = xb_add(&bar[XB_TOP], 1u);
;             const unsigned tg = og / nx;
;             if (og + 1u == (tg + 1u) * nx) xb_add(&bar[XB_TOPGEN], 1u);
;             else XB_SPIN(xb_ld(&bar[XB_TOPGEN]) == tg, bar);
.LBB0_1451:
	s_or_b64 exec, exec, s[20:21]
	v_cvt_f32_u32_e32 v4, v1
	s_waitcnt vmcnt(0)
	v_readfirstlane_b32 s18, v3
	s_add_u32 s20, s70, 0x4500
	s_addc_u32 s21, s71, 0
	v_rcp_iflag_f32_e32 v4, v4
	v_add_u32_e32 v2, s18, v2
	v_add_u32_e32 v5, 1, v2
	s_mov_b64 s[22:23], 0
	v_mul_f32_e32 v3, 0x4f7ffffe, v4
	v_cvt_u32_f32_e32 v3, v3
	v_sub_u32_e32 v4, 0, v1
	v_mul_lo_u32 v4, v4, v3
	v_mul_hi_u32 v4, v3, v4
	v_add_u32_e32 v3, v3, v4
	v_mul_hi_u32 v3, v2, v3
	v_mul_lo_u32 v4, v3, v1
	v_sub_u32_e32 v2, v2, v4
	v_add_u32_e32 v6, 1, v3
	v_cmp_ge_u32_e32 vcc, v2, v1
	v_sub_u32_e32 v4, v2, v1
	s_nop 0
	v_cndmask_b32_e32 v3, v3, v6, vcc
	v_cndmask_b32_e32 v2, v2, v4, vcc
	v_add_u32_e32 v4, 1, v3
	v_cmp_ge_u32_e32 vcc, v2, v1
	s_nop 1
	v_cndmask_b32_e32 v4, v3, v4, vcc
	v_mul_lo_u32 v2, v1, v4
	v_add_u32_e32 v1, v2, v1
	v_cmp_ne_u32_e32 vcc, v5, v1
	v_mov_b32_e32 v5, v1
	v_mov_b64_e32 v[2:3], s[20:21]
	s_and_saveexec_b64 s[18:19], vcc
	s_cbranch_execz .LBB0_1463
	v_mov_b32_e32 v1, 0
	global_load_dword v2, v1, s[20:21] offset:-256 sc1
	s_mov_b64 s[36:37], 0
	s_waitcnt vmcnt(0)
	v_cmp_lt_u32_e32 vcc, v2, v5
	s_and_saveexec_b64 s[26:27], vcc
	s_cbranch_execz .LBB0_1462
	s_add_u32 s22, s70, 0x1200
	s_addc_u32 s23, s71, 0
	s_mov_b32 s24, 1
	s_branch .LBB0_1455

; __device__ __forceinline__ unsigned xb_ld(unsigned* p)              { return __hip_atomic_load(p, __ATOMIC_RELAXED, __HIP_MEMORY_SCOPE_AGENT); }
; __device__ __forceinline__ unsigned xb_add(unsigned* p, unsigned v) { return __hip_atomic_fetch_add(p, v, __ATOMIC_RELAXED, __HIP_MEMORY_SCOPE_AGENT); }
; #define XB_SPIN(cond, bar) do { unsigned _sp = 0; while (cond) { __builtin_amdgcn_s_sleep(1); \
;     if ((++_sp & 255u) == 0u) { if (xb_ld(&(bar)[XB_TMO])) break; if (_sp > XB_SPIN_CAP) { atomicAdd(&(bar)[XB_TMO], 1u); break; } } } } while (0)
; __device__ __forceinline__ void xcd_barrier(const XcdBarrier& b) {
;     ...
;             xb_add(&bar[XB_XGEN(b.x)], 1u);
;             __builtin_amdgcn_fence(__ATOMIC_ACQUIRE, "agent");
;         } else {
;             XB_SPIN(xb_ld(&bar[XB_XGEN(b.x)]) == gen, bar);
;             __builtin_amdgcn_fence(__ATOMIC_ACQUIRE, "agent");
.LBB0_1465:
	s_or_b64 exec, exec, s[18:19]
	s_mov_b64 s[20:21], exec
	v_mbcnt_lo_u32_b32 v1, s20, 0
	v_mbcnt_hi_u32_b32 v1, s21, v1
	v_cmp_eq_u32_e32 vcc, 0, v1
	s_and_saveexec_b64 s[18:19], vcc
	s_cbranch_execz .LBB0_1467
	s_bcnt1_i32_b64 s20, s[20:21]
	v_mov_b32_e32 v1, 0x2000
	v_mov_b32_e32 v2, s20
.LBB0_1467:
	s_or_b64 exec, exec, s[18:19]
	s_waitcnt vmcnt(0)
	buffer_inv sc1

; __device__ __forceinline__ unsigned xb_ld(unsigned* p)              { return __hip_atomic_load(p, __ATOMIC_RELAXED, __HIP_MEMORY_SCOPE_AGENT); }
; __device__ __forceinline__ unsigned xb_add(unsigned* p, unsigned v) { return __hip_atomic_fetch_add(p, v, __ATOMIC_RELAXED, __HIP_MEMORY_SCOPE_AGENT); }
; #define XB_SPIN(cond, bar) do { unsigned _sp = 0; while (cond) { __builtin_amdgcn_s_sleep(1); \
;     if ((++_sp & 255u) == 0u) { if (xb_ld(&(bar)[XB_TMO])) break; if (_sp > XB_SPIN_CAP) { atomicAdd(&(bar)[XB_TMO], 1u); break; } } } } while (0)
; __device__ __forceinline__ void xcd_barrier(const XcdBarrier& b) {
;     ...
;         const unsigned old = xb_add(&bar[XB_XSUB(b.x)], 1u);
;         const unsigned gen = old / nloc;
;         if (old + 1u == (gen + 1u) * nloc) {
;             __builtin_amdgcn_fence(__ATOMIC_RELEASE, "agent");
;             asm volatile("s_waitcnt vmcnt(0)" ::: "memory");
;             const unsigned og = xb_add(&bar[XB_TOP], 1u);
;             const unsigned tg = og / nx;
;             if (og + 1u == (tg + 1u) * nx) xb_add(&bar[XB_TOPGEN], 1u);
;             else XB_SPIN(xb_ld(&bar[XB_TOPGEN]) == tg, bar);
.LBB0_1539:
	s_or_b64 exec, exec, s[12:13]
	v_cvt_f32_u32_e32 v4, v1
	s_waitcnt vmcnt(0)
	v_readfirstlane_b32 s8, v3
	s_add_u32 s12, s70, 0x4500
	s_addc_u32 s13, s71, 0
	v_rcp_iflag_f32_e32 v4, v4
	v_add_u32_e32 v2, s8, v2
	v_add_u32_e32 v5, 1, v2
	s_mov_b64 s[14:15], 0
	v_mul_f32_e32 v3, 0x4f7ffffe, v4
	v_cvt_u32_f32_e32 v3, v3
	v_sub_u32_e32 v4, 0, v1
	v_mul_lo_u32 v4, v4, v3
	v_mul_hi_u32 v4, v3, v4
	v_add_u32_e32 v3, v3, v4
	v_mul_hi_u32 v3, v2, v3
	v_mul_lo_u32 v4, v3, v1
	v_sub_u32_e32 v2, v2, v4
	v_add_u32_e32 v6, 1, v3
	v_cmp_ge_u32_e32 vcc, v2, v1
	v_sub_u32_e32 v4, v2, v1
	s_nop 0
	v_cndmask_b32_e32 v3, v3, v6, vcc
	v_cndmask_b32_e32 v2, v2, v4, vcc
	v_add_u32_e32 v4, 1, v3
	v_cmp_ge_u32_e32 vcc, v2, v1
	s_nop 1
	v_cndmask_b32_e32 v4, v3, v4, vcc
	v_mul_lo_u32 v2, v1, v4
	v_add_u32_e32 v1, v2, v1
	v_cmp_ne_u32_e32 vcc, v5, v1
	v_mov_b32_e32 v5, v1
	v_mov_b64_e32 v[2:3], s[12:13]
	s_and_saveexec_b64 s[8:9], vcc
	s_cbranch_execz .LBB0_1551
	v_mov_b32_e32 v1, 0
	global_load_dword v2, v1, s[12:13] offset:-256 sc1
	s_mov_b64 s[18:19], 0
	s_waitcnt vmcnt(0)
	v_cmp_lt_u32_e32 vcc, v2, v5
	s_and_saveexec_b64 s[16:17], vcc
	s_cbranch_execz .LBB0_1550
	s_add_u32 s14, s70, 0x1200
	s_addc_u32 s15, s71, 0
	s_mov_b32 s24, 1
	s_branch .LBB0_1543

; __device__ __forceinline__ unsigned xb_ld(unsigned* p)              { return __hip_atomic_load(p, __ATOMIC_RELAXED, __HIP_MEMORY_SCOPE_AGENT); }
; __device__ __forceinline__ unsigned xb_add(unsigned* p, unsigned v) { return __hip_atomic_fetch_add(p, v, __ATOMIC_RELAXED, __HIP_MEMORY_SCOPE_AGENT); }
; #define XB_SPIN(cond, bar) do { unsigned _sp = 0; while (cond) { __builtin_amdgcn_s_sleep(1); \
;     if ((++_sp & 255u) == 0u) { if (xb_ld(&(bar)[XB_TMO])) break; if (_sp > XB_SPIN_CAP) { atomicAdd(&(bar)[XB_TMO], 1u); break; } } } } while (0)
; __device__ __forceinline__ void xcd_barrier(const XcdBarrier& b) {
;     ...
;             xb_add(&bar[XB_XGEN(b.x)], 1u);
;             __builtin_amdgcn_fence(__ATOMIC_ACQUIRE, "agent");
;         } else {
;             XB_SPIN(xb_ld(&bar[XB_XGEN(b.x)]) == gen, bar);
;             __builtin_amdgcn_fence(__ATOMIC_ACQUIRE, "agent");
.LBB0_1553:
	s_or_b64 exec, exec, s[8:9]
	s_mov_b64 s[12:13], exec
	v_mbcnt_lo_u32_b32 v1, s12, 0
	v_mbcnt_hi_u32_b32 v1, s13, v1
	v_cmp_eq_u32_e32 vcc, 0, v1
	s_and_saveexec_b64 s[8:9], vcc
	s_cbranch_execz .LBB0_1555
	s_bcnt1_i32_b64 s12, s[12:13]
	v_mov_b32_e32 v1, 0x2000
	v_mov_b32_e32 v2, s12
.LBB0_1555:
	s_or_b64 exec, exec, s[8:9]
	s_waitcnt vmcnt(0)
	buffer_inv sc1
